# unused
# baseline (speedup 1.0000x reference)
; __device__ __forceinline__ int tid_fresh() { int t = threadIdx.x; asm volatile("" : "+v"(t)); return t; }
; #define PG8_STAGE(bufoff, gbase, v0, v1) do { \
;         __builtin_amdgcn_global_load_lds((const unsigned*)((const char*)(gbase) + (v0)), (LAS unsigned*)(lds + (bufoff) + ldsw), 16, 0, 0); \
;         __builtin_amdgcn_global_load_lds((const unsigned*)((const char*)(gbase) + (v1)), (LAS unsigned*)(lds + (bufoff) + ldsw + 8192), 16, 0, 0); } while (0)
; template <class Epi, class Sched>
; __device__ __forceinline__ void gemm_phase(LAS unsigned char* lds, const int K, const Sched& S, const Epi& E) {
;     const int tid = tid_fresh(), wid = __builtin_amdgcn_readfirstlane(tid >> 6), lane = tid & 63, wr = wid >> 2, wc = wid & 3, fr = lane & 15, fq = lane >> 4;
;     const int nt = K / BK;
;     int R0, C0, R1, C1; stage_rc(tid * 16, R0, C0); stage_rc(tid * 16 + 8192, R1, C1);
;     const int Rb0 = Epi::PERM ? ((R0 & ~31) + perm32(R0 & 31)) : R0, Rb1 = Epi::PERM ? ((R1 & ~31) + perm32(R1 & 31)) : R1;
;     const unsigned voffB0 = S.b_off(Rb0, C0), voffB1 = S.b_off(Rb1, C1);
;     const size_t kstep = (size_t)(BK * 2);
;     const size_t kstepB = S.b_kstep(), hstep = S.b_hstep();
;     const unsigned ldsw = (unsigned)wid * 1024u;
;     const int aoff = lds_byte(wr * 64 + fr, fq * 8), boff = lds_byte(wc * 32 + fr, fq * 8);
;     ...
;     Unit cur, nxt; int ui = 0;
;     if (!S.next(0, cur)) return;
;     f32x4 acc[2][2][4][2];
; #pragma unroll
;     for (int a = 0; a < 2; ++a)
; #pragma unroll
;         for (int b = 0; b < 2; ++b)
; #pragma unroll
;             for (int m = 0; m < 4; ++m)
; #pragma unroll
;                 for (int n = 0; n < 2; ++n) acc[a][b][m][n] = (f32x4){0.f, 0.f, 0.f, 0.f};
;     bf16x8 At[4][2], B0[2][2], B1[2][2];
;     const char* const gA = S.a_base();
;     unsigned c00, c01, c10, c11, n00, n01, n10, n11;
;     PG8_AOFFS(cur, c00, c01, c10, c11);
;     const char* cB = S.b_ptr(cur);
;     PG8_STAGE(PG8_SB(0, 0), cB, voffB0, voffB1); PG8_STAGE(PG8_SA(0, 0), gA, c00, c01); PG8_STAGE(PG8_SB(0, 1), cB + hstep, voffB0, voffB1); PG8_STAGE(PG8_SA(0, 1), gA, c10, c11);
;     if (wr == 1) PG8_BAR;
;     PG8_WAIT_V(4); PG8_BAR;
;     PG8_STAGE(PG8_SB(1, 0), cB + kstepB, voffB0, voffB1); PG8_STAGE(PG8_SA(1, 0), gA + kstep, c00, c01); PG8_STAGE(PG8_SB(1, 1), cB + hstep + kstepB, voffB0, voffB1);
;     PG8_WAIT_V(6); PG8_BAR;
.LBB0_237:
	s_or_b64 exec, exec, s[0:1]
	v_readlane_b32 s3, v254, 5
	s_cmpk_lt_i32 s3, 0x300
	v_readlane_b32 s2, v254, 4
	v_readlane_b32 s0, v254, 0
	s_cselect_b64 s[4:5], -1, 0
	s_ashr_i32 s2, s2, 31
	v_readlane_b32 s1, v254, 1
	v_writelane_b32 v254, s2, 11
	s_ashr_i32 s2, s3, 31
	v_writelane_b32 v254, s2, 15
	s_waitcnt vmcnt(10)
	v_mov_b32_e32 v6, v0
	v_writelane_b32 v254, s4, 17
	s_waitcnt lgkmcnt(0)
	s_barrier
	v_readlane_b32 s84, v254, 0
	v_readlane_b32 s85, v254, 1
	s_nop 1
	s_load_dwordx2 s[74:75], s[84:85], 0xe8
	s_load_dwordx2 s[78:79], s[84:85], 0x118
	v_and_b32_e32 v252, 63, v0
	v_lshrrev_b32_e32 v253, 6, v0
	v_lshlrev_b32_e32 v238, 2, v252
	v_lshlrev_b32_e32 v252, 4, v252
	v_add_u32_e32 v239, 0x2000, v238
	v_add_u32_e32 v240, 0x4000, v238
	v_add_u32_e32 v241, 0x6000, v238
	v_readlane_b32 s86, v254, 4
	v_readlane_b32 s87, v255, 40
	v_readfirstlane_b32 s88, v253
	s_nop 3
	s_lshl_b32 s71, s86, 3
	s_lshl_b32 s87, s87, 3
	s_add_u32 s87, s87, s88
	s_add_u32 s70, s87, 0x28000
	s_mov_b32 s80, 0
	s_mov_b32 s82, 0
	s_mov_b32 s90, 0
	s_waitcnt lgkmcnt(0)
	v_writelane_b32 v254, s5, 18
	v_readfirstlane_b32 s13, v6
	s_and_b64 vcc, exec, s[4:5]
	s_cbranch_vccz .LBB0_251
	v_ashrrev_i32_e32 v1, 31, v6
	v_lshrrev_b32_e32 v1, 26, v1
	v_add_u32_e32 v1, v6, v1
	v_ashrrev_i32_e32 v3, 6, v1
	v_bfe_i32 v1, v6, 27, 1
	v_lshlrev_b32_e32 v2, 4, v6
	v_lshrrev_b32_e32 v1, 22, v1
	v_add_u32_e32 v1, v2, v1
	v_and_b32_e32 v1, 0xfffffc00, v1
	v_sub_u32_e32 v1, v2, v1
	v_lshrrev_b32_e32 v4, 4, v1
	v_bitop3_b32 v4, v4, v1, 32 bitop3:0x6c
	v_ashrrev_i32_e32 v1, 31, v1
	v_lshrrev_b32_e32 v1, 26, v1
	v_lshlrev_b32_e32 v5, 3, v3
	v_add_u32_e32 v1, v4, v1
	v_and_b32_e32 v5, -16, v5
	v_ashrrev_i32_e32 v7, 6, v1
	v_add_u32_e32 v2, 0x2000, v2
	v_add_u32_e32 v1, v7, v5
	v_ashrrev_i32_e32 v5, 31, v2
	v_lshrrev_b32_e32 v5, 22, v5
	v_add_u32_e32 v5, v2, v5
	v_ashrrev_i32_e32 v5, 10, v5
	v_mul_i32_i24_e32 v8, 0x400, v5
	v_sub_u32_e32 v2, v2, v8
	v_lshrrev_b32_e32 v8, 4, v2
	v_bitop3_b32 v2, v8, v2, 32 bitop3:0x6c
	v_ashrrev_i32_e32 v9, 31, v2
	s_load_dwordx2 s[4:5], s[0:1], 0x118
	v_lshrrev_b32_e32 v9, 26, v9
	v_add_u32_e32 v9, v2, v9
	s_waitcnt vmcnt(9)
	v_ashrrev_i32_e32 v10, 6, v9
	v_and_b32_e32 v9, 0xc0, v9
	v_sub_u32_e32 v2, v2, v9
	v_mov_b32_e32 v9, 1
	v_lshlrev_b32_e32 v8, 3, v5
	v_lshlrev_b32_e32 v5, 5, v5
	v_ashrrev_i16_sdwa v2, v9, sext(v2) dst_sel:DWORD dst_unused:UNUSED_PAD src0_sel:DWORD src1_sel:BYTE_0
	s_waitcnt lgkmcnt(0)
	s_add_u32 s6, s4, 0x34c30000
	v_and_b32_e32 v8, -16, v8
	v_and_b32_e32 v5, 32, v5
	v_bfe_i32 v2, v2, 0, 16
	s_addc_u32 s7, s5, 0
	v_add_u32_e32 v150, v10, v8
	v_and_b32_e32 v8, 3, v10
	s_mov_b32 s0, 0xfffe0
	v_add_lshl_u32 v151, v5, v2, 1
	v_and_b32_e32 v2, 3, v7
	s_add_u32 s17, s4, 0x30000
	v_and_or_b32 v8, v150, s0, v8
	v_and_or_b32 v2, v1, s0, v2
	v_readlane_b32 s0, v254, 15
	s_addc_u32 s26, s5, 0
	s_lshr_b32 s0, s0, 29
	v_readlane_b32 s8, v254, 5
	s_add_i32 s0, s8, s0
	s_ashr_i32 s2, s13, 6
	s_ashr_i32 s3, s0, 3
	s_and_b32 s0, s0, -8
	s_ashr_i32 s1, s13, 8
	s_lshl_b32 s27, s2, 10
	s_sub_i32 s0, s8, s0
	s_cmp_lt_i32 s0, 0
	s_movk_i32 s28, 0x61
	s_cselect_b32 s8, s28, 0x60
	s_mul_i32 s0, s8, s0
	s_add_i32 s0, s0, s3
	s_mul_hi_i32 s3, s0, 0x2aaaaaab
	s_lshr_b32 s8, s3, 31
	s_ashr_i32 s3, s3, 5
	s_add_i32 s3, s3, s8
	s_mul_i32 s8, s3, 0xc0
	s_sub_i32 s8, s0, s8
	v_lshrrev_b32_e32 v10, 2, v150
	v_lshlrev_b32_e32 v11, 1, v150
	s_bfe_u32 s0, s8, 0x3001c
	v_and_b32_e32 v10, 4, v10
	v_and_b32_e32 v11, 24, v11
	s_add_i32 s9, s8, s0
	v_or3_b32 v8, v8, v10, v11
	s_sext_i32_i16 s0, s9
	s_and_b32 s9, s9, 0xfff8
	v_lshl_add_u32 v130, v8, 12, v151
	v_lshrrev_b32_e32 v5, 2, v1
	v_lshlrev_b32_e32 v8, 1, v1
	s_sub_i32 s8, s8, s9
	v_and_b32_e32 v5, 4, v5
	v_and_b32_e32 v8, 24, v8
	s_sext_i32_i16 s8, s8
	v_or3_b32 v2, v2, v5, v8
	v_mul_i32_i24_e32 v5, 64, v7
	s_lshr_b32 s0, s0, 3
	s_lshl_b32 s3, s3, 11
	s_lshl_b32 s8, s8, 8
	v_sub_u32_e32 v4, v4, v5
	s_add_i32 s43, s8, s3
	s_bfe_i64 s[8:9], s[0:1], 0x100000
	v_lshlrev_b32_e32 v3, 5, v3
	v_ashrrev_i16_sdwa v4, v9, sext(v4) dst_sel:DWORD dst_unused:UNUSED_PAD src0_sel:DWORD src1_sel:BYTE_0
	s_lshl_b64 s[8:9], s[8:9], 20
	v_and_b32_e32 v3, 32, v3
	v_bfe_i32 v4, v4, 0, 16
	s_add_u32 s20, s17, s8
	v_add_lshl_u32 v152, v3, v4, 1
	s_addc_u32 s21, s26, s9
	s_add_i32 s29, s27, 0
	v_lshl_add_u32 v132, v2, 12, v152
	s_add_i32 m0, s29, 0x10000
	v_add_u32_e32 v2, s43, v1
	global_load_lds_dwordx4 v132, s[20:21]
	s_add_i32 m0, s29, 0x12000
	v_add_u32_e32 v3, s43, v150
	v_lshl_add_u32 v134, v2, 12, v152
	global_load_lds_dwordx4 v130, s[20:21]
	s_mov_b32 m0, s29
	s_add_i32 s30, s29, 0x2000
	v_lshl_add_u32 v140, v3, 12, v151
	global_load_lds_dwordx4 v134, s[6:7]
	s_mov_b32 m0, s30
	s_add_u32 s8, s20, 0x80000
	v_add_u32_e32 v153, 0x80, v1
	global_load_lds_dwordx4 v140, s[6:7]
	s_addc_u32 s9, s21, 0
	s_add_i32 m0, s29, 0x14000
	v_add_u32_e32 v4, s43, v153
	v_add_u32_e32 v154, 0x80, v150
	global_load_lds_dwordx4 v132, s[8:9]
	s_add_i32 m0, s29, 0x16000
	s_add_i32 s31, s29, 0x4000
	v_add_u32_e32 v5, s43, v154
	v_lshl_add_u32 v142, v4, 12, v152
	global_load_lds_dwordx4 v130, s[8:9]
	s_mov_b32 m0, s31
	s_add_i32 s33, s29, 0x6000
	v_lshl_add_u32 v144, v5, 12, v151
	global_load_lds_dwordx4 v142, s[6:7]
	s_mov_b32 m0, s33
	v_mov_b32_e32 v135, 0
	global_load_lds_dwordx4 v144, s[6:7]
	v_mov_b32_e32 v133, v135
	v_mov_b32_e32 v131, v135
	s_mov_b32 s34, 0
	v_lshl_add_u64 v[4:5], s[20:21], 0, v[132:133]
	v_lshl_add_u64 v[2:3], s[20:21], 0, v[130:131]
	s_cmp_lg_u32 s1, 1
	v_mov_b32_e32 v141, v135
	s_cbranch_scc1 .LBB0_240
	s_barrier

; #define PG8_STAGE(bufoff, gbase, v0, v1) do { \
;         __builtin_amdgcn_global_load_lds((const unsigned*)((const char*)(gbase) + (v0)), (LAS unsigned*)(lds + (bufoff) + ldsw), 16, 0, 0); \
;         __builtin_amdgcn_global_load_lds((const unsigned*)((const char*)(gbase) + (v1)), (LAS unsigned*)(lds + (bufoff) + ldsw + 8192), 16, 0, 0); } while (0)
; #define PG8_LDA(dst, b, h) do { _Pragma("unroll") for (int m = 0; m < 4; ++m) _Pragma("unroll") for (int k = 0; k < 2; ++k) dst[m][k] = *(const LAS bf16x8*)(lds + PG8_SA(b, h) + aoff + m * 2048 + k * 1024); } while (0)
; #define PG8_LDB(dst, b, h) do { _Pragma("unroll") for (int n = 0; n < 2; ++n) _Pragma("unroll") for (int k = 0; k < 2; ++k) dst[n][k] = *(const LAS bf16x8*)(lds + PG8_SB(b, h) + boff + n * 2048 + k * 1024); } while (0)
; #define PG8_MMA(ai, bj, At, Bt) do { __builtin_amdgcn_s_setprio(1); _Pragma("unroll") for (int m = 0; m < 4; ++m) _Pragma("unroll") for (int n = 0; n < 2; ++n) _Pragma("unroll") for (int k = 0; k < 2; ++k) \
;         acc[ai][bj][m][n] = __builtin_amdgcn_mfma_f32_16x16x32_bf16(Bt[n][k], At[m][k], acc[ai][bj][m][n], 0, 0, 0); __builtin_amdgcn_s_setprio(0); } while (0)
; #define PG8_WAIT_V(n) asm volatile("s_waitcnt vmcnt(" #n ")" ::: "memory")
; #define PG8_WAIT_L(n) asm volatile("s_waitcnt lgkmcnt(" #n ")" ::: "memory")
; #define PG8_BAR __builtin_amdgcn_s_barrier()
; #define PG8_SCHED __builtin_amdgcn_sched_barrier(0)
; template <class Epi, class Sched>
; __device__ __forceinline__ void gemm_phase(LAS unsigned char* lds, const int K, const Sched& S, const Epi& E) {
;     ...
;             PG8_LDB(B0, 0, 0); PG8_SCHED; PG8_LDA(At, 0, 0); PG8_STAGE(PG8_SA(1, 1), a1, c10, c11);
;             PG8_WAIT_L(8); PG8_BAR; PG8_WAIT_L(0); PG8_MMA(0, 0, At, B0); PG8_BAR; PG8_SCHED;
;             PG8_LDB(B1, 0, 1); PG8_STAGE(PG8_SB(0, 0), b2, voffB0, voffB1);
;             PG8_BAR; PG8_WAIT_L(0); PG8_MMA(0, 1, At, B1); PG8_BAR;
;             PG8_LDA(At, 0, 1); PG8_STAGE(PG8_SA(0, 0), a2, x00, x01);
;             PG8_BAR; PG8_WAIT_L(0); PG8_MMA(1, 0, At, B0); PG8_BAR; PG8_SCHED;
;             PG8_STAGE(PG8_SB(0, 1), b2 + hstep, voffB0, voffB1);
;             PG8_WAIT_V(6); PG8_BAR; PG8_MMA(1, 1, At, B1); PG8_BAR;
.LBB0_246:
	s_add_u32 s22, s4, s20
	s_addc_u32 s23, s5, s21
	s_add_u32 s24, s22, 0x34c30100
	ds_read_b128 v[166:169], v158
	ds_read_b128 v[170:173], v158 offset:1024
	ds_read_b128 v[174:177], v158 offset:2048
	ds_read_b128 v[178:181], v158 offset:3072
	s_addc_u32 s25, s23, 0
	s_add_u32 s47, s19, s20
	s_addc_u32 s48, s45, s21
	s_cmpk_eq_i32 s20, 0xf00
	s_cselect_b64 vcc, -1, 0
	s_and_b64 s[22:23], vcc, exec
	v_cndmask_b32_e32 v134, v141, v161, vcc
	s_cselect_b32 s25, s7, s25
	s_cselect_b32 s24, s6, s24
	v_cndmask_b32_e32 v143, v142, v163, vcc
	s_cselect_b32 s23, s3, s48
	s_cselect_b32 s22, s2, s47
	v_cndmask_b32_e32 v206, v140, v162, vcc
	s_mov_b32 m0, s40
	v_lshl_add_u64 v[216:217], v[148:149], 0, s[20:21]
	ds_read_b128 v[182:185], v159
	ds_read_b128 v[186:189], v159 offset:1024
	ds_read_b128 v[190:193], v159 offset:2048
	ds_read_b128 v[194:197], v159 offset:3072
	ds_read_b128 v[198:201], v159 offset:4096
	ds_read_b128 v[202:205], v159 offset:5120
	ds_read_b128 v[208:211], v159 offset:6144
	ds_read_b128 v[212:215], v159 offset:7168
	global_load_lds_dwordx4 v[216:217], off
	v_lshl_add_u64 v[216:217], v[146:147], 0, s[20:21]
	s_add_i32 m0, s29, 0xe000
	s_nop 0
	global_load_lds_dwordx4 v[216:217], off
	s_waitcnt lgkmcnt(8)
	s_barrier
	s_waitcnt lgkmcnt(0)
	s_setprio 1
	s_waitcnt lgkmcnt(0)
	v_mfma_f32_16x16x32_bf16 v[126:129], v[166:169], v[182:185], v[126:129]
	v_mfma_f32_16x16x32_bf16 v[122:125], v[174:177], v[182:185], v[122:125]
	v_mfma_f32_16x16x32_bf16 v[118:121], v[166:169], v[190:193], v[118:121]
	v_mfma_f32_16x16x32_bf16 v[110:113], v[174:177], v[190:193], v[110:113]
	v_mfma_f32_16x16x32_bf16 v[102:105], v[166:169], v[198:201], v[102:105]
	v_mfma_f32_16x16x32_bf16 v[94:97], v[174:177], v[198:201], v[94:97]
	v_mfma_f32_16x16x32_bf16 v[86:89], v[166:169], v[208:211], v[86:89]
	v_mfma_f32_16x16x32_bf16 v[78:81], v[174:177], v[208:211], v[78:81]
	v_mfma_f32_16x16x32_bf16 v[126:129], v[170:173], v[186:189], v[126:129]
	v_mfma_f32_16x16x32_bf16 v[122:125], v[178:181], v[186:189], v[122:125]
	v_mfma_f32_16x16x32_bf16 v[118:121], v[170:173], v[194:197], v[118:121]
	v_mfma_f32_16x16x32_bf16 v[110:113], v[178:181], v[194:197], v[110:113]
	v_mfma_f32_16x16x32_bf16 v[102:105], v[170:173], v[202:205], v[102:105]
	v_mfma_f32_16x16x32_bf16 v[94:97], v[178:181], v[202:205], v[94:97]
	v_mfma_f32_16x16x32_bf16 v[86:89], v[170:173], v[212:215], v[86:89]
	v_mfma_f32_16x16x32_bf16 v[78:81], v[178:181], v[212:215], v[78:81]
	s_setprio 0
	s_barrier
	s_add_i32 s47, s37, s27
	v_lshl_add_u64 v[232:233], s[22:23], 0, v[132:133]
	s_mov_b32 m0, s47
	ds_read_b128 v[216:219], v160
	ds_read_b128 v[220:223], v160 offset:1024
	ds_read_b128 v[224:227], v160 offset:2048
	ds_read_b128 v[228:231], v160 offset:3072
	global_load_lds_dwordx4 v[232:233], off
	v_lshl_add_u64 v[234:235], s[22:23], 0, v[130:131]
	s_add_i32 m0, s47, 0x2000
	s_nop 0
	global_load_lds_dwordx4 v[234:235], off
	s_barrier
	s_waitcnt lgkmcnt(0)
	s_setprio 1
	s_waitcnt lgkmcnt(0)
	v_mfma_f32_16x16x32_bf16 v[114:117], v[216:219], v[182:185], v[114:117]
	v_mfma_f32_16x16x32_bf16 v[106:109], v[224:227], v[182:185], v[106:109]
	v_mfma_f32_16x16x32_bf16 v[98:101], v[216:219], v[190:193], v[98:101]
	v_mfma_f32_16x16x32_bf16 v[90:93], v[224:227], v[190:193], v[90:93]
	v_mfma_f32_16x16x32_bf16 v[82:85], v[216:219], v[198:201], v[82:85]
	v_mfma_f32_16x16x32_bf16 v[74:77], v[224:227], v[198:201], v[74:77]
	v_mfma_f32_16x16x32_bf16 v[70:73], v[216:219], v[208:211], v[70:73]
	v_mfma_f32_16x16x32_bf16 v[66:69], v[224:227], v[208:211], v[66:69]
	v_mfma_f32_16x16x32_bf16 v[114:117], v[220:223], v[186:189], v[114:117]
	v_mfma_f32_16x16x32_bf16 v[106:109], v[228:231], v[186:189], v[106:109]
	v_mfma_f32_16x16x32_bf16 v[98:101], v[220:223], v[194:197], v[98:101]
	v_mfma_f32_16x16x32_bf16 v[90:93], v[228:231], v[194:197], v[90:93]
	v_mfma_f32_16x16x32_bf16 v[82:85], v[220:223], v[202:205], v[82:85]
	v_mfma_f32_16x16x32_bf16 v[74:77], v[228:231], v[202:205], v[74:77]
	v_mfma_f32_16x16x32_bf16 v[70:73], v[220:223], v[212:215], v[70:73]
	v_mfma_f32_16x16x32_bf16 v[66:69], v[228:231], v[212:215], v[66:69]
	s_setprio 0
	s_mov_b32 m0, s29
	s_barrier
	ds_read_b128 v[182:185], v159 offset:16384
	ds_read_b128 v[186:189], v159 offset:17408
	ds_read_b128 v[190:193], v159 offset:18432
	ds_read_b128 v[194:197], v159 offset:19456
	ds_read_b128 v[198:201], v159 offset:20480
	ds_read_b128 v[202:205], v159 offset:21504
	ds_read_b128 v[208:211], v159 offset:22528
	ds_read_b128 v[212:215], v159 offset:23552
	global_load_lds_dwordx4 v134, s[24:25]
	s_mov_b32 m0, s30
	v_mov_b32_e32 v207, v135
	global_load_lds_dwordx4 v206, s[24:25]
	s_barrier
	s_waitcnt lgkmcnt(0)
	v_lshl_add_u64 v[236:237], s[24:25], 0, v[134:135]
	v_lshl_add_u64 v[206:207], s[24:25], 0, v[206:207]
	s_setprio 1
	s_waitcnt lgkmcnt(0)
	v_mfma_f32_16x16x32_bf16 v[62:65], v[166:169], v[182:185], v[62:65]
	v_mfma_f32_16x16x32_bf16 v[58:61], v[174:177], v[182:185], v[58:61]
	v_mfma_f32_16x16x32_bf16 v[54:57], v[166:169], v[190:193], v[54:57]
	v_mfma_f32_16x16x32_bf16 v[46:49], v[174:177], v[190:193], v[46:49]
	v_mfma_f32_16x16x32_bf16 v[38:41], v[166:169], v[198:201], v[38:41]
	v_mfma_f32_16x16x32_bf16 v[30:33], v[174:177], v[198:201], v[30:33]
	v_mfma_f32_16x16x32_bf16 v[22:25], v[166:169], v[208:211], v[22:25]
	v_mfma_f32_16x16x32_bf16 v[14:17], v[174:177], v[208:211], v[14:17]
	v_mfma_f32_16x16x32_bf16 v[62:65], v[170:173], v[186:189], v[62:65]
	v_mfma_f32_16x16x32_bf16 v[58:61], v[178:181], v[186:189], v[58:61]
	v_mfma_f32_16x16x32_bf16 v[54:57], v[170:173], v[194:197], v[54:57]
	v_mfma_f32_16x16x32_bf16 v[46:49], v[178:181], v[194:197], v[46:49]
	v_mfma_f32_16x16x32_bf16 v[38:41], v[170:173], v[202:205], v[38:41]
	v_mfma_f32_16x16x32_bf16 v[30:33], v[178:181], v[202:205], v[30:33]
	v_mfma_f32_16x16x32_bf16 v[22:25], v[170:173], v[212:215], v[22:25]
	v_mfma_f32_16x16x32_bf16 v[14:17], v[178:181], v[212:215], v[14:17]
	s_setprio 0
	s_barrier
	s_add_u32 s48, s22, 0x80000
	s_addc_u32 s49, s23, 0
	s_add_i32 s47, s38, s27
	v_lshl_add_u64 v[166:167], s[48:49], 0, v[132:133]
	s_mov_b32 m0, s47
	s_nop 0
	global_load_lds_dwordx4 v[166:167], off
	v_lshl_add_u64 v[166:167], s[48:49], 0, v[130:131]
	s_add_i32 m0, s47, 0x2000
	s_nop 0
	global_load_lds_dwordx4 v[166:167], off
	s_cmp_eq_u32 s82, 0
	s_cbranch_scc1 .Lpb2_p4n
	s_waitcnt vmcnt(14)
	v_cvt_pk_bf16_f32 v244, v244, v245
	v_cvt_pk_bf16_f32 v245, v246, v247
	v_cvt_pk_bf16_f32 v246, v248, v249
	v_cvt_pk_bf16_f32 v247, v250, v251
	global_store_dwordx4 v253, v[244:247], s[78:79] nt
	s_mov_b32 s82, 0
	s_waitcnt vmcnt(7)
	s_branch .Lpb2_p4j

; #define PG8_STAGE(bufoff, gbase, v0, v1) do { \
;         __builtin_amdgcn_global_load_lds((const unsigned*)((const char*)(gbase) + (v0)), (LAS unsigned*)(lds + (bufoff) + ldsw), 16, 0, 0); \
;         __builtin_amdgcn_global_load_lds((const unsigned*)((const char*)(gbase) + (v1)), (LAS unsigned*)(lds + (bufoff) + ldsw + 8192), 16, 0, 0); } while (0)
; #define PG8_LDA(dst, b, h) do { _Pragma("unroll") for (int m = 0; m < 4; ++m) _Pragma("unroll") for (int k = 0; k < 2; ++k) dst[m][k] = *(const LAS bf16x8*)(lds + PG8_SA(b, h) + aoff + m * 2048 + k * 1024); } while (0)
; #define PG8_LDB(dst, b, h) do { _Pragma("unroll") for (int n = 0; n < 2; ++n) _Pragma("unroll") for (int k = 0; k < 2; ++k) dst[n][k] = *(const LAS bf16x8*)(lds + PG8_SB(b, h) + boff + n * 2048 + k * 1024); } while (0)
; #define PG8_MMA(ai, bj, At, Bt) do { __builtin_amdgcn_s_setprio(1); _Pragma("unroll") for (int m = 0; m < 4; ++m) _Pragma("unroll") for (int n = 0; n < 2; ++n) _Pragma("unroll") for (int k = 0; k < 2; ++k) \
;         acc[ai][bj][m][n] = __builtin_amdgcn_mfma_f32_16x16x32_bf16(Bt[n][k], At[m][k], acc[ai][bj][m][n], 0, 0, 0); __builtin_amdgcn_s_setprio(0); } while (0)
; #define PG8_WAIT_V(n) asm volatile("s_waitcnt vmcnt(" #n ")" ::: "memory")
; #define PG8_BAR __builtin_amdgcn_s_barrier()
; #define PG8_SCHED __builtin_amdgcn_sched_barrier(0)
; template <class Epi, class Sched>
; __device__ __forceinline__ void gemm_phase(LAS unsigned char* lds, const int K, const Sched& S, const Epi& E) {
;     ...
;             PG8_WAIT_V(6); PG8_BAR; PG8_MMA(1, 1, At, B1); PG8_BAR;
;             PG8_LDB(B0, 1, 0); PG8_SCHED; PG8_LDA(At, 1, 0); PG8_STAGE(PG8_SA(0, 1), a2, x10, x11);
; __device__ __forceinline__ bool bg_decode(int st, int wg, int NW, int lane, KP kp, const float*& src, int& ldS, bf16_t*& dst, int& o2) {
;     ...
;         const int r2 = r - 65536, e = r2 >> 9, kc = (r2 >> 3) & 63, cc = r2 & 7, n = cc * 256 + lane;
;         ldS = D; o2 = 128 * 8;
;         src = kp->in[29] + ((size_t)(l * NE + e) * FF + kc * 8) * D + n;
;         dst = (bf16_t*)(ws + WS_WD) + l * WD_L + (size_t)e * D * FF + ((size_t)kc * D + n) * 8;
.Lpb2_p4j:
	s_barrier
	s_setprio 1
	v_mfma_f32_16x16x32_bf16 v[50:53], v[216:219], v[182:185], v[50:53]
	v_mfma_f32_16x16x32_bf16 v[42:45], v[224:227], v[182:185], v[42:45]
	v_mfma_f32_16x16x32_bf16 v[34:37], v[216:219], v[190:193], v[34:37]
	v_mfma_f32_16x16x32_bf16 v[26:29], v[224:227], v[190:193], v[26:29]
	v_mfma_f32_16x16x32_bf16 v[18:21], v[216:219], v[198:201], v[18:21]
	v_mfma_f32_16x16x32_bf16 v[10:13], v[224:227], v[198:201], v[10:13]
	v_mfma_f32_16x16x32_bf16 v[6:9], v[216:219], v[208:211], v[6:9]
	v_mfma_f32_16x16x32_bf16 v[2:5], v[224:227], v[208:211], v[2:5]
	v_mfma_f32_16x16x32_bf16 v[50:53], v[220:223], v[186:189], v[50:53]
	v_mfma_f32_16x16x32_bf16 v[42:45], v[228:231], v[186:189], v[42:45]
	v_mfma_f32_16x16x32_bf16 v[34:37], v[220:223], v[194:197], v[34:37]
	v_mfma_f32_16x16x32_bf16 v[26:29], v[228:231], v[194:197], v[26:29]
	v_mfma_f32_16x16x32_bf16 v[18:21], v[220:223], v[202:205], v[18:21]
	v_mfma_f32_16x16x32_bf16 v[10:13], v[228:231], v[202:205], v[10:13]
	v_mfma_f32_16x16x32_bf16 v[6:9], v[220:223], v[212:215], v[6:9]
	v_mfma_f32_16x16x32_bf16 v[2:5], v[228:231], v[212:215], v[2:5]
	s_setprio 0
	s_add_i32 s47, 0, 0x18000
	v_add_u32_e32 v134, s47, v156
	s_barrier
	ds_read_b128 v[166:169], v134
	ds_read_b128 v[170:173], v134 offset:1024
	ds_read_b128 v[174:177], v134 offset:2048
	ds_read_b128 v[178:181], v134 offset:3072
	s_mov_b32 m0, s31
	ds_read_b128 v[182:185], v159 offset:32768
	ds_read_b128 v[186:189], v159 offset:33792
	ds_read_b128 v[190:193], v159 offset:34816
	ds_read_b128 v[194:197], v159 offset:35840
	ds_read_b128 v[198:201], v159 offset:36864
	ds_read_b128 v[202:205], v159 offset:37888
	ds_read_b128 v[208:211], v159 offset:38912
	ds_read_b128 v[212:215], v159 offset:39936
	v_cndmask_b32_e32 v134, v144, v164, vcc
	global_load_lds_dwordx4 v143, s[24:25]
	s_mov_b32 m0, s33
	s_nop 0
	global_load_lds_dwordx4 v134, s[24:25]
	s_cmp_ge_u32 s70, 0x2e000
	s_cbranch_scc1 .Lpb2_p5n
	s_cmp_eq_u32 s80, 0
	s_cbranch_scc0 .Lpb2_adv2
	s_cmp_ge_u32 s70, 0x28000
	s_mov_b32 s84, 0x10000
	s_cselect_b32 s84, 0x28000, s84
	s_cselect_b32 s83, 0x10000000, 0
	s_mov_b32 s81, 0x24830000
	s_cselect_b32 s81, 0x2ca30000, s81
	s_sub_u32 s84, s70, s84
	s_lshr_b32 s85, s84, 3
	s_and_b32 s86, s84, 7
	s_lshl_b32 s87, s85, 16
	s_lshl_b32 s84, s86, 10
	s_add_u32 s87, s87, s84
	s_add_u32 s87, s87, s83
	s_add_u32 s72, s74, s87
	s_addc_u32 s73, s75, 0
	s_add_u32 s88, s72, 0x8000
	s_addc_u32 s89, s73, 0
	s_lshl_b32 s85, s85, 15
	s_lshl_b32 s86, s86, 12
	s_add_u32 s85, s85, s86
	s_add_u32 s85, s85, s81
	v_add_u32_e32 v253, s85, v252
	s_branch .Lpb2_ld2

; #define PG8_STAGE(bufoff, gbase, v0, v1) do { \
;         __builtin_amdgcn_global_load_lds((const unsigned*)((const char*)(gbase) + (v0)), (LAS unsigned*)(lds + (bufoff) + ldsw), 16, 0, 0); \
;         __builtin_amdgcn_global_load_lds((const unsigned*)((const char*)(gbase) + (v1)), (LAS unsigned*)(lds + (bufoff) + ldsw + 8192), 16, 0, 0); } while (0)
; #define PG8_LDA(dst, b, h) do { _Pragma("unroll") for (int m = 0; m < 4; ++m) _Pragma("unroll") for (int k = 0; k < 2; ++k) dst[m][k] = *(const LAS bf16x8*)(lds + PG8_SA(b, h) + aoff + m * 2048 + k * 1024); } while (0)
; #define PG8_LDB(dst, b, h) do { _Pragma("unroll") for (int n = 0; n < 2; ++n) _Pragma("unroll") for (int k = 0; k < 2; ++k) dst[n][k] = *(const LAS bf16x8*)(lds + PG8_SB(b, h) + boff + n * 2048 + k * 1024); } while (0)
; #define PG8_MMA(ai, bj, At, Bt) do { __builtin_amdgcn_s_setprio(1); _Pragma("unroll") for (int m = 0; m < 4; ++m) _Pragma("unroll") for (int n = 0; n < 2; ++n) _Pragma("unroll") for (int k = 0; k < 2; ++k) \
;         acc[ai][bj][m][n] = __builtin_amdgcn_mfma_f32_16x16x32_bf16(Bt[n][k], At[m][k], acc[ai][bj][m][n], 0, 0, 0); __builtin_amdgcn_s_setprio(0); } while (0)
; #define PG8_WAIT_V(n) asm volatile("s_waitcnt vmcnt(" #n ")" ::: "memory")
; #define PG8_WAIT_L(n) asm volatile("s_waitcnt lgkmcnt(" #n ")" ::: "memory")
; #define PG8_BAR __builtin_amdgcn_s_barrier()
; #define PG8_SCHED __builtin_amdgcn_sched_barrier(0)
; template <class Epi, class Sched>
; __device__ __forceinline__ void gemm_phase(LAS unsigned char* lds, const int K, const Sched& S, const Epi& E) {
;     ...
;             PG8_WAIT_L(8); PG8_BAR; PG8_WAIT_L(0); PG8_MMA(0, 0, At, B0); PG8_BAR; PG8_SCHED;
;             PG8_LDB(B1, 1, 1); PG8_STAGE(PG8_SB(1, 0), b3, voffB0, voffB1);
;             PG8_BAR; PG8_WAIT_L(0); PG8_MMA(0, 1, At, B1); PG8_BAR;
;             PG8_LDA(At, 1, 1); PG8_STAGE(PG8_SA(1, 0), a3, x00, x01);
;             PG8_BAR; PG8_WAIT_L(0); PG8_MMA(1, 0, At, B0); PG8_BAR; PG8_SCHED;
;             PG8_STAGE(PG8_SB(1, 1), b3 + hstep, voffB0, voffB1);
;             PG8_WAIT_V(6); PG8_BAR; PG8_MMA(1, 1, At, B1); PG8_BAR;
.Lpb2_p5n:
	s_waitcnt lgkmcnt(8)
	s_barrier
	s_waitcnt lgkmcnt(0)
	s_setprio 1
	s_waitcnt lgkmcnt(0)
	v_mfma_f32_16x16x32_bf16 v[126:129], v[166:169], v[182:185], v[126:129]
	v_mfma_f32_16x16x32_bf16 v[122:125], v[174:177], v[182:185], v[122:125]
	v_mfma_f32_16x16x32_bf16 v[118:121], v[166:169], v[190:193], v[118:121]
	v_mfma_f32_16x16x32_bf16 v[110:113], v[174:177], v[190:193], v[110:113]
	v_mfma_f32_16x16x32_bf16 v[102:105], v[166:169], v[198:201], v[102:105]
	v_mfma_f32_16x16x32_bf16 v[94:97], v[174:177], v[198:201], v[94:97]
	v_mfma_f32_16x16x32_bf16 v[86:89], v[166:169], v[208:211], v[86:89]
	v_mfma_f32_16x16x32_bf16 v[78:81], v[174:177], v[208:211], v[78:81]
	v_mfma_f32_16x16x32_bf16 v[126:129], v[170:173], v[186:189], v[126:129]
	v_mfma_f32_16x16x32_bf16 v[122:125], v[178:181], v[186:189], v[122:125]
	v_mfma_f32_16x16x32_bf16 v[118:121], v[170:173], v[194:197], v[118:121]
	v_mfma_f32_16x16x32_bf16 v[110:113], v[178:181], v[194:197], v[110:113]
	v_mfma_f32_16x16x32_bf16 v[102:105], v[170:173], v[202:205], v[102:105]
	v_mfma_f32_16x16x32_bf16 v[94:97], v[178:181], v[202:205], v[94:97]
	v_mfma_f32_16x16x32_bf16 v[86:89], v[170:173], v[212:215], v[86:89]
	v_mfma_f32_16x16x32_bf16 v[78:81], v[178:181], v[212:215], v[78:81]
	s_setprio 0
	s_barrier
	s_add_i32 s24, 0, 0x1c000
	s_add_i32 s25, s47, s27
	v_add_u32_e32 v134, s24, v156
	v_lshl_add_u64 v[232:233], v[232:233], 0, s[14:15]
	s_mov_b32 m0, s25
	ds_read_b128 v[216:219], v134
	ds_read_b128 v[220:223], v134 offset:1024
	ds_read_b128 v[224:227], v134 offset:2048
	ds_read_b128 v[228:231], v134 offset:3072
	global_load_lds_dwordx4 v[232:233], off
	v_lshl_add_u64 v[232:233], v[234:235], 0, s[14:15]
	s_add_i32 m0, s25, 0x2000
	s_nop 0
	global_load_lds_dwordx4 v[232:233], off
	s_barrier
	s_waitcnt lgkmcnt(0)
	s_setprio 1
	s_waitcnt lgkmcnt(0)
	v_mfma_f32_16x16x32_bf16 v[114:117], v[216:219], v[182:185], v[114:117]
	v_mfma_f32_16x16x32_bf16 v[106:109], v[224:227], v[182:185], v[106:109]
	v_mfma_f32_16x16x32_bf16 v[98:101], v[216:219], v[190:193], v[98:101]
	v_mfma_f32_16x16x32_bf16 v[90:93], v[224:227], v[190:193], v[90:93]
	v_mfma_f32_16x16x32_bf16 v[82:85], v[216:219], v[198:201], v[82:85]
	v_mfma_f32_16x16x32_bf16 v[74:77], v[224:227], v[198:201], v[74:77]
	v_mfma_f32_16x16x32_bf16 v[70:73], v[216:219], v[208:211], v[70:73]
	v_mfma_f32_16x16x32_bf16 v[66:69], v[224:227], v[208:211], v[66:69]
	v_mfma_f32_16x16x32_bf16 v[114:117], v[220:223], v[186:189], v[114:117]
	v_mfma_f32_16x16x32_bf16 v[106:109], v[228:231], v[186:189], v[106:109]
	v_mfma_f32_16x16x32_bf16 v[98:101], v[220:223], v[194:197], v[98:101]
	v_mfma_f32_16x16x32_bf16 v[90:93], v[228:231], v[194:197], v[90:93]
	v_mfma_f32_16x16x32_bf16 v[82:85], v[220:223], v[202:205], v[82:85]
	v_mfma_f32_16x16x32_bf16 v[74:77], v[228:231], v[202:205], v[74:77]
	v_mfma_f32_16x16x32_bf16 v[70:73], v[220:223], v[212:215], v[70:73]
	v_mfma_f32_16x16x32_bf16 v[66:69], v[228:231], v[212:215], v[66:69]
	s_setprio 0
	s_mov_b32 m0, s35
	v_lshl_add_u64 v[232:233], v[236:237], 0, s[14:15]
	s_barrier
	ds_read_b128 v[182:185], v159 offset:49152
	ds_read_b128 v[186:189], v159 offset:50176
	ds_read_b128 v[190:193], v159 offset:51200
	ds_read_b128 v[194:197], v159 offset:52224
	ds_read_b128 v[198:201], v159 offset:53248
	ds_read_b128 v[202:205], v159 offset:54272
	ds_read_b128 v[208:211], v159 offset:55296
	ds_read_b128 v[212:215], v159 offset:56320
	global_load_lds_dwordx4 v[232:233], off
	v_lshl_add_u64 v[206:207], v[206:207], 0, s[14:15]
	s_mov_b32 m0, s36
	s_nop 0
	global_load_lds_dwordx4 v[206:207], off
	s_barrier
	s_waitcnt lgkmcnt(0)
	s_setprio 1
	s_waitcnt lgkmcnt(0)
	v_mfma_f32_16x16x32_bf16 v[62:65], v[166:169], v[182:185], v[62:65]
	v_mfma_f32_16x16x32_bf16 v[58:61], v[174:177], v[182:185], v[58:61]
	v_mfma_f32_16x16x32_bf16 v[54:57], v[166:169], v[190:193], v[54:57]
	v_mfma_f32_16x16x32_bf16 v[46:49], v[174:177], v[190:193], v[46:49]
	v_mfma_f32_16x16x32_bf16 v[38:41], v[166:169], v[198:201], v[38:41]
	v_mfma_f32_16x16x32_bf16 v[30:33], v[174:177], v[198:201], v[30:33]
	v_mfma_f32_16x16x32_bf16 v[22:25], v[166:169], v[208:211], v[22:25]
	v_mfma_f32_16x16x32_bf16 v[14:17], v[174:177], v[208:211], v[14:17]
	v_mfma_f32_16x16x32_bf16 v[62:65], v[170:173], v[186:189], v[62:65]
	v_mfma_f32_16x16x32_bf16 v[58:61], v[178:181], v[186:189], v[58:61]
	v_mfma_f32_16x16x32_bf16 v[54:57], v[170:173], v[194:197], v[54:57]
	v_mfma_f32_16x16x32_bf16 v[46:49], v[178:181], v[194:197], v[46:49]
	v_mfma_f32_16x16x32_bf16 v[38:41], v[170:173], v[202:205], v[38:41]
	v_mfma_f32_16x16x32_bf16 v[30:33], v[178:181], v[202:205], v[30:33]
	v_mfma_f32_16x16x32_bf16 v[22:25], v[170:173], v[212:215], v[22:25]
	v_mfma_f32_16x16x32_bf16 v[14:17], v[178:181], v[212:215], v[14:17]
	s_setprio 0
	s_barrier
	s_add_u32 s22, s22, 0x80080
	s_addc_u32 s23, s23, 0
	s_add_i32 s24, s24, s27
	v_lshl_add_u64 v[166:167], s[22:23], 0, v[132:133]
	s_mov_b32 m0, s24
	s_nop 0
	global_load_lds_dwordx4 v[166:167], off
	v_lshl_add_u64 v[166:167], s[22:23], 0, v[130:131]
	s_add_i32 m0, s24, 0x2000
	s_nop 0
	global_load_lds_dwordx4 v[166:167], off
	s_cmp_eq_u32 s82, 0
	s_cbranch_scc1 .Lpb2_p8n
	s_waitcnt vmcnt(14)
	s_branch .Lpb2_p8j

; __device__ __forceinline__ unsigned cvt_pk_bf16(float lo, float hi) { unsigned r; asm volatile("v_cvt_pk_bf16_f32 %0, %1, %2" : "=v"(r) : "v"(lo), "v"(hi)); return r; }
; #define PG8_MMA(ai, bj, At, Bt) do { __builtin_amdgcn_s_setprio(1); _Pragma("unroll") for (int m = 0; m < 4; ++m) _Pragma("unroll") for (int n = 0; n < 2; ++n) _Pragma("unroll") for (int k = 0; k < 2; ++k) \
;         acc[ai][bj][m][n] = __builtin_amdgcn_mfma_f32_16x16x32_bf16(Bt[n][k], At[m][k], acc[ai][bj][m][n], 0, 0, 0); __builtin_amdgcn_s_setprio(0); } while (0)
; #define PG8_WAIT_V(n) asm volatile("s_waitcnt vmcnt(" #n ")" ::: "memory")
; #define PG8_BAR __builtin_amdgcn_s_barrier()
; template <class Epi, class Sched>
; __device__ __forceinline__ void gemm_phase(LAS unsigned char* lds, const int K, const Sched& S, const Epi& E) {
;     ...
;             PG8_WAIT_V(6); PG8_BAR; PG8_MMA(1, 1, At, B1); PG8_BAR;
;         }
;         E(acc, cur, wr, wc, fr, fq);
;         if (!has_next) break;
;     __device__ __forceinline__ void operator()(const f32x4 (&acc)[2][2][4][2], const Unit& u, int wr, int wc, int fr, int fq) const {
;         const int row0 = u.rbase + wr * 64 + fr, col0 = u.pn * BM + wc * 32 + 8 * fq;
; #pragma unroll
;         for (int ai = 0; ai < 2; ++ai)
; #pragma unroll
;             for (int m = 0; m < 4; ++m) { bf16_t* rowp = O + (size_t)(row0 + ai * HALF + m * 16) * ldc + col0;
; #pragma unroll
;                 for (int bj = 0; bj < 2; ++bj) { const f32x4 v0 = acc[ai][bj][m][0], v1 = acc[ai][bj][m][1];
;                     u32x4 w; w.x = cvt_pk_bf16(v0[0], v0[1]); w.y = cvt_pk_bf16(v0[2], v0[3]); w.z = cvt_pk_bf16(v1[0], v1[1]); w.w = cvt_pk_bf16(v1[2], v1[3]);
;                     *(u32x4*)(rowp + bj * HALF) = w; } }
.Lpb2_p8j:
	s_barrier
	s_setprio 1
	v_mfma_f32_16x16x32_bf16 v[50:53], v[216:219], v[182:185], v[50:53]
	v_mfma_f32_16x16x32_bf16 v[42:45], v[224:227], v[182:185], v[42:45]
	v_mfma_f32_16x16x32_bf16 v[34:37], v[216:219], v[190:193], v[34:37]
	v_mfma_f32_16x16x32_bf16 v[26:29], v[224:227], v[190:193], v[26:29]
	v_mfma_f32_16x16x32_bf16 v[18:21], v[216:219], v[198:201], v[18:21]
	v_mfma_f32_16x16x32_bf16 v[10:13], v[224:227], v[198:201], v[10:13]
	v_mfma_f32_16x16x32_bf16 v[6:9], v[216:219], v[208:211], v[6:9]
	v_mfma_f32_16x16x32_bf16 v[2:5], v[224:227], v[208:211], v[2:5]
	v_mfma_f32_16x16x32_bf16 v[50:53], v[220:223], v[186:189], v[50:53]
	v_mfma_f32_16x16x32_bf16 v[42:45], v[228:231], v[186:189], v[42:45]
	v_mfma_f32_16x16x32_bf16 v[34:37], v[220:223], v[194:197], v[34:37]
	v_mfma_f32_16x16x32_bf16 v[26:29], v[228:231], v[194:197], v[26:29]
	v_mfma_f32_16x16x32_bf16 v[18:21], v[220:223], v[202:205], v[18:21]
	v_mfma_f32_16x16x32_bf16 v[10:13], v[228:231], v[202:205], v[10:13]
	v_mfma_f32_16x16x32_bf16 v[6:9], v[220:223], v[212:215], v[6:9]
	v_mfma_f32_16x16x32_bf16 v[2:5], v[228:231], v[212:215], v[2:5]
	s_setprio 0
	s_add_i32 s46, s46, 2
	s_add_u32 s20, s20, 0x100
	s_addc_u32 s21, s21, 0
	s_cmp_gt_u32 s46, 29
	s_barrier
	s_cbranch_scc0 .LBB0_246
	v_lshl_or_b32 v142, s44, 8, v157
	v_add_u32_e32 v134, s43, v155
	v_ashrrev_i32_e32 v143, 31, v142
	v_mov_b64_e32 v[140:141], s[8:9]
	v_mad_i64_i32 v[144:145], s[20:21], v134, s39, v[140:141]
	v_lshlrev_b64 v[142:143], 1, v[142:143]
	v_lshl_add_u64 v[144:145], v[144:145], 0, v[142:143]
	v_cvt_pk_bf16_f32 v126, v126, v127
	v_cvt_pk_bf16_f32 v127, v128, v129
	v_cvt_pk_bf16_f32 v128, v122, v123
	v_cvt_pk_bf16_f32 v129, v124, v125
	global_store_dwordx4 v[144:145], v[126:129], off
	v_cvt_pk_bf16_f32 v114, v114, v115
	v_cvt_pk_bf16_f32 v115, v116, v117
	v_cvt_pk_bf16_f32 v116, v106, v107
	v_add_u32_e32 v106, 16, v134
	v_mad_i64_i32 v[106:107], s[20:21], v106, s39, v[140:141]
	v_cvt_pk_bf16_f32 v117, v108, v109
	global_store_dwordx4 v[144:145], v[114:117], off offset:256
	s_and_b64 vcc, exec, s[0:1]
	s_mov_b32 s44, s18
	v_lshl_add_u64 v[114:115], v[106:107], 0, v[142:143]
	v_cvt_pk_bf16_f32 v106, v118, v119
	v_cvt_pk_bf16_f32 v107, v120, v121
	v_cvt_pk_bf16_f32 v108, v110, v111
	v_cvt_pk_bf16_f32 v109, v112, v113
	global_store_dwordx4 v[114:115], v[106:109], off
	v_cvt_pk_bf16_f32 v98, v98, v99
	v_cvt_pk_bf16_f32 v99, v100, v101
	v_cvt_pk_bf16_f32 v100, v90, v91
	v_add_u32_e32 v90, 32, v134
	v_mad_i64_i32 v[90:91], s[20:21], v90, s39, v[140:141]
	v_cvt_pk_bf16_f32 v101, v92, v93
	global_store_dwordx4 v[114:115], v[98:101], off offset:256
	s_mov_b32 s43, s41
	v_mov_b32_e32 v144, v164
	v_lshl_add_u64 v[98:99], v[90:91], 0, v[142:143]
	v_cvt_pk_bf16_f32 v90, v102, v103
	v_cvt_pk_bf16_f32 v91, v104, v105
	v_cvt_pk_bf16_f32 v92, v94, v95
	v_cvt_pk_bf16_f32 v93, v96, v97
	global_store_dwordx4 v[98:99], v[90:93], off
	v_cvt_pk_bf16_f32 v82, v82, v83
	v_cvt_pk_bf16_f32 v83, v84, v85
	v_cvt_pk_bf16_f32 v84, v74, v75
	v_add_u32_e32 v74, 48, v134
	v_mad_i64_i32 v[74:75], s[20:21], v74, s39, v[140:141]
	v_cvt_pk_bf16_f32 v85, v76, v77
	global_store_dwordx4 v[98:99], v[82:85], off offset:256
	s_nop 1
	v_lshl_add_u64 v[82:83], v[74:75], 0, v[142:143]
	v_cvt_pk_bf16_f32 v74, v86, v87
	v_cvt_pk_bf16_f32 v75, v88, v89
	v_cvt_pk_bf16_f32 v76, v78, v79
	v_cvt_pk_bf16_f32 v77, v80, v81
	global_store_dwordx4 v[82:83], v[74:77], off
	v_cvt_pk_bf16_f32 v70, v70, v71
	v_cvt_pk_bf16_f32 v71, v72, v73
	v_cvt_pk_bf16_f32 v72, v66, v67
	v_add_u32_e32 v66, 0x80, v134
	v_mad_i64_i32 v[66:67], s[20:21], v66, s39, v[140:141]
	v_lshl_add_u64 v[66:67], v[66:67], 0, v[142:143]
	v_cvt_pk_bf16_f32 v73, v68, v69
	global_store_dwordx4 v[82:83], v[70:73], off offset:256
	v_cvt_pk_bf16_f32 v62, v62, v63
	v_cvt_pk_bf16_f32 v63, v64, v65
	v_cvt_pk_bf16_f32 v64, v58, v59
	v_cvt_pk_bf16_f32 v65, v60, v61
	global_store_dwordx4 v[66:67], v[62:65], off
	v_cvt_pk_bf16_f32 v50, v50, v51
	v_cvt_pk_bf16_f32 v51, v52, v53
	v_cvt_pk_bf16_f32 v52, v42, v43
	v_add_u32_e32 v42, 0x90, v134
	v_mad_i64_i32 v[42:43], s[20:21], v42, s39, v[140:141]
	v_cvt_pk_bf16_f32 v53, v44, v45
	global_store_dwordx4 v[66:67], v[50:53], off offset:256
	s_nop 1
	v_lshl_add_u64 v[50:51], v[42:43], 0, v[142:143]
	v_cvt_pk_bf16_f32 v42, v54, v55
	v_cvt_pk_bf16_f32 v43, v56, v57
	v_cvt_pk_bf16_f32 v44, v46, v47
	v_cvt_pk_bf16_f32 v45, v48, v49
	global_store_dwordx4 v[50:51], v[42:45], off
	v_cvt_pk_bf16_f32 v34, v34, v35
	v_cvt_pk_bf16_f32 v35, v36, v37
	v_cvt_pk_bf16_f32 v36, v26, v27
	v_add_u32_e32 v26, 0xa0, v134
	v_mad_i64_i32 v[26:27], s[20:21], v26, s39, v[140:141]
	v_cvt_pk_bf16_f32 v37, v28, v29
	global_store_dwordx4 v[50:51], v[34:37], off offset:256
	s_nop 1
	v_lshl_add_u64 v[34:35], v[26:27], 0, v[142:143]
	v_cvt_pk_bf16_f32 v26, v38, v39
	v_cvt_pk_bf16_f32 v27, v40, v41
	v_cvt_pk_bf16_f32 v28, v30, v31
	v_cvt_pk_bf16_f32 v29, v32, v33
	global_store_dwordx4 v[34:35], v[26:29], off
	v_cvt_pk_bf16_f32 v18, v18, v19
	v_cvt_pk_bf16_f32 v19, v20, v21
	v_cvt_pk_bf16_f32 v20, v10, v11
	v_add_u32_e32 v10, 0xb0, v134
	v_mad_i64_i32 v[10:11], s[20:21], v10, s39, v[140:141]
	v_cvt_pk_bf16_f32 v21, v12, v13
	global_store_dwordx4 v[34:35], v[18:21], off offset:256
	v_mov_b32_e32 v141, v161
	v_mov_b32_e32 v140, v162
	v_lshl_add_u64 v[18:19], v[10:11], 0, v[142:143]
	v_mov_b32_e32 v142, v163
	s_mov_b64 s[20:21], s[2:3]
	v_cvt_pk_bf16_f32 v10, v22, v23
	v_cvt_pk_bf16_f32 v11, v24, v25
	v_cvt_pk_bf16_f32 v12, v14, v15
	v_cvt_pk_bf16_f32 v13, v16, v17
	global_store_dwordx4 v[18:19], v[10:13], off
	v_cvt_pk_bf16_f32 v6, v6, v7
	v_cvt_pk_bf16_f32 v7, v8, v9
	v_cvt_pk_bf16_f32 v8, v2, v3
	v_cvt_pk_bf16_f32 v9, v4, v5
	global_store_dwordx4 v[18:19], v[6:9], off offset:256
	s_cbranch_vccz .LBB0_241
	s_waitcnt vmcnt(0)
	s_cmpk_gt_u32 s13, 0xff
	s_cbranch_scc1 .LBB0_250
	s_barrier

; #define BG_I(x) bg_issue1<x>(bg, bgwg, bgNW, bglane)
; #define BG_F(y) bg_finish1<y, 32>(bg)
; __device__ __forceinline__ bool bg_decode(int st, int wg, int NW, int lane, KP kp, const float*& src, int& ldS, bf16_t*& dst, int& o2) {
;     ...
;         const int r2 = r - 65536, e = r2 >> 9, kc = (r2 >> 3) & 63, cc = r2 & 7, n = cc * 256 + lane;
;         ldS = D; o2 = 128 * 8;
;         src = kp->in[29] + ((size_t)(l * NE + e) * FF + kc * 8) * D + n;
;         dst = (bf16_t*)(ws + WS_WD) + l * WD_L + (size_t)e * D * FF + ((size_t)kc * D + n) * 8;
; __device__ __forceinline__ void hy_fft_phase(LAS unsigned char* lds, int bid, int G, const bf16_t* vgT, bf16_t* zT, const float* a3, const float* wout, const float* skip, float* filt, float4* gspec) {
;     ...
;     { const int nst = (BG_STEPS + bgNW - 1) / bgNW;
;       if (bg.st < nst) { BG_I(0);
; #pragma unroll 1
;         while (bg.st < nst) { BG_I(1); BG_F(0); BG_I(0); BG_F(1); }
;         bg_finish1<0, 0>(bg); } }
.Lpb2_d1:
	s_cmp_ge_u32 s70, 0x2e000
	s_cbranch_scc1 .Lpb2_dend
	s_cmp_eq_u32 s80, 0
	s_cbranch_scc0 .Lpb2_adv1
	s_cmp_ge_u32 s70, 0x28000
	s_mov_b32 s84, 0x10000
	s_cselect_b32 s84, 0x28000, s84
	s_cselect_b32 s83, 0x10000000, 0
	s_mov_b32 s81, 0x24830000
	s_cselect_b32 s81, 0x2ca30000, s81
	s_sub_u32 s84, s70, s84
	s_lshr_b32 s85, s84, 3
	s_and_b32 s86, s84, 7
	s_lshl_b32 s87, s85, 16
	s_lshl_b32 s84, s86, 10
	s_add_u32 s87, s87, s84
	s_add_u32 s87, s87, s83
	s_add_u32 s72, s74, s87
	s_addc_u32 s73, s75, 0
	s_add_u32 s88, s72, 0x8000
	s_addc_u32 s89, s73, 0
	s_lshl_b32 s85, s85, 15
	s_lshl_b32 s86, s86, 12
	s_add_u32 s85, s85, s86
	s_add_u32 s85, s85, s81
	v_add_u32_e32 v253, s85, v252
	s_branch .Lpb2_ld1

; __device__ __forceinline__ void xcd_barrier(const XcdBarrier& b) {
;     asm volatile("s_waitcnt vmcnt(0)" ::: "memory");
;     __syncthreads();
;     if (threadIdx.x == 0) {
;         unsigned* bar = b.bar;
;         __builtin_amdgcn_s_waitcnt(0);
;         unsigned nloc = b.st[0], nx = b.st[1];
;         if (nloc == 0u) { xcd_barrier_complete(bar, b.x, nloc, nx); b.st[0] = nloc; b.st[1] = nx; }
; template <int BANK> __device__ __forceinline__ void bg_issue1(BgState& b, int wg, int NW, int lane) {
;     ...
;     for (int i = 0; i < 8; ++i) { const float* p = src + (size_t)i * ldS;
;         asm volatile("global_load_dword %0, %4, off\n\tglobal_load_dword %1, %4, off offset:256\n\tglobal_load_dword %2, %4, off offset:512\n\tglobal_load_dword %3, %4, off offset:768"
;                      : "=&v"(b.r[(BANK * 8 + i) * 4 + 0]), "=&v"(b.r[(BANK * 8 + i) * 4 + 1]), "=&v"(b.r[(BANK * 8 + i) * 4 + 2]), "=&v"(b.r[(BANK * 8 + i) * 4 + 3]) : "v"(p) : "memory"); }
;     b.st += 1;
.Lpb2_ld1:
	global_load_dword v244, v238, s[72:73] nt
	global_load_dword v245, v239, s[72:73] nt
	global_load_dword v246, v240, s[72:73] nt
	global_load_dword v247, v241, s[72:73] nt
	global_load_dword v248, v238, s[88:89] nt
	global_load_dword v249, v239, s[88:89] nt
	global_load_dword v250, v240, s[88:89] nt
	global_load_dword v251, v241, s[88:89] nt
	s_add_u32 s80, s80, 1
	s_and_b32 s80, s80, 3
	s_cmp_eq_u32 s80, 0
	s_cselect_b32 s84, s71, 0
	s_add_u32 s70, s70, s84
	s_mov_b32 s82, 1
	s_branch .Lpb2_drain
.Lpb2_dend:
	s_waitcnt vmcnt(0)
	s_waitcnt vmcnt(0) lgkmcnt(0)
	s_barrier
	s_mov_b64 s[0:1], exec
	v_readlane_b32 s2, v254, 9
	v_readlane_b32 s3, v254, 10
	s_and_b64 s[2:3], s[0:1], s[2:3]
	s_xor_b64 s[0:1], s[2:3], s[0:1]
	s_mov_b64 exec, s[2:3]
	s_cbranch_execz .LBB0_304
	s_add_i32 s2, 0, 0x21000
	v_mov_b32_e32 v1, s2
	s_waitcnt vmcnt(0) expcnt(0) lgkmcnt(0)
	ds_read_b32 v3, v1
	s_add_i32 s2, 0, 0x21004
	v_mov_b32_e32 v1, s2
	ds_read_b32 v1, v1
	s_waitcnt lgkmcnt(1)
	v_cmp_ne_u32_e32 vcc, 0, v3
	s_cbranch_vccnz .LBB0_267
	v_readlane_b32 s2, v254, 2
	v_readlane_b32 s3, v254, 3
	s_load_dwordx2 s[6:7], s[2:3], 0x4
	v_readlane_b32 s8, v254, 6
	v_readlane_b32 s9, v254, 7
	s_add_u32 s2, s8, 0x1000
	s_addc_u32 s3, s9, 0
	s_add_u32 s4, s8, 0x1100
	s_addc_u32 s5, s9, 0
	v_readlane_b32 s10, v254, 4
	s_waitcnt lgkmcnt(0)
	s_mul_i32 s13, s6, s10
	s_add_u32 s6, s8, 0x1200
	s_mul_i32 s13, s13, s7
	s_addc_u32 s7, s9, 0
	s_add_u32 s8, s8, 0x1300
	s_addc_u32 s9, s9, 0
	s_mov_b32 s17, 1
	v_mov_b32_e32 v17, 0
	s_branch .LBB0_255

; __device__ __forceinline__ int tid_fresh() { int t = threadIdx.x; asm volatile("" : "+v"(t)); return t; }
; #define PG8_STAGE(bufoff, gbase, v0, v1) do { \
;         __builtin_amdgcn_global_load_lds((const unsigned*)((const char*)(gbase) + (v0)), (LAS unsigned*)(lds + (bufoff) + ldsw), 16, 0, 0); \
;         __builtin_amdgcn_global_load_lds((const unsigned*)((const char*)(gbase) + (v1)), (LAS unsigned*)(lds + (bufoff) + ldsw + 8192), 16, 0, 0); } while (0)
; template <class Epi, class Sched>
; __device__ __forceinline__ void gemm_phase(LAS unsigned char* lds, const int K, const Sched& S, const Epi& E) {
;     const int tid = tid_fresh(), wid = __builtin_amdgcn_readfirstlane(tid >> 6), lane = tid & 63, wr = wid >> 2, wc = wid & 3, fr = lane & 15, fq = lane >> 4;
;     const int nt = K / BK;
;     int R0, C0, R1, C1; stage_rc(tid * 16, R0, C0); stage_rc(tid * 16 + 8192, R1, C1);
;     const int Rb0 = Epi::PERM ? ((R0 & ~31) + perm32(R0 & 31)) : R0, Rb1 = Epi::PERM ? ((R1 & ~31) + perm32(R1 & 31)) : R1;
;     const unsigned voffB0 = S.b_off(Rb0, C0), voffB1 = S.b_off(Rb1, C1);
;     const size_t kstep = (size_t)(BK * 2);
;     const size_t kstepB = S.b_kstep(), hstep = S.b_hstep();
;     const unsigned ldsw = (unsigned)wid * 1024u;
;     const int aoff = lds_byte(wr * 64 + fr, fq * 8), boff = lds_byte(wc * 32 + fr, fq * 8);
;     ...
;     Unit cur, nxt; int ui = 0;
;     if (!S.next(0, cur)) return;
;     f32x4 acc[2][2][4][2];
; #pragma unroll
;     for (int a = 0; a < 2; ++a)
; #pragma unroll
;         for (int b = 0; b < 2; ++b)
; #pragma unroll
;             for (int m = 0; m < 4; ++m)
; #pragma unroll
;                 for (int n = 0; n < 2; ++n) acc[a][b][m][n] = (f32x4){0.f, 0.f, 0.f, 0.f};
;     bf16x8 At[4][2], B0[2][2], B1[2][2];
;     const char* const gA = S.a_base();
;     unsigned c00, c01, c10, c11, n00, n01, n10, n11;
;     PG8_AOFFS(cur, c00, c01, c10, c11);
;     const char* cB = S.b_ptr(cur);
;     PG8_STAGE(PG8_SB(0, 0), cB, voffB0, voffB1); PG8_STAGE(PG8_SA(0, 0), gA, c00, c01); PG8_STAGE(PG8_SB(0, 1), cB + hstep, voffB0, voffB1); PG8_STAGE(PG8_SA(0, 1), gA, c10, c11);
;     if (wr == 1) PG8_BAR;
;     PG8_WAIT_V(4); PG8_BAR;
;     PG8_STAGE(PG8_SB(1, 0), cB + kstepB, voffB0, voffB1); PG8_STAGE(PG8_SA(1, 0), gA + kstep, c00, c01); PG8_STAGE(PG8_SB(1, 1), cB + hstep + kstepB, voffB0, voffB1);
;     PG8_WAIT_V(6); PG8_BAR;
.LBB0_1152:
	s_or_b64 exec, exec, s[0:1]
	v_readlane_b32 s0, v254, 0
	v_readlane_b32 s2, v254, 5
	v_readlane_b32 s1, v254, 1
	s_lshl_b32 s15, s28, 3
	s_and_b32 s3, s2, 7
	v_mov_b32_e32 v2, v0
	s_waitcnt lgkmcnt(0)
	s_barrier
	v_readlane_b32 s84, v254, 0
	v_readlane_b32 s85, v254, 1
	s_nop 1
	s_load_dwordx2 s[74:75], s[84:85], 0xd8
	s_load_dwordx2 s[76:77], s[84:85], 0xe0
	s_load_dwordx2 s[78:79], s[84:85], 0x118
	v_and_b32_e32 v252, 63, v0
	v_lshrrev_b32_e32 v253, 6, v0
	v_lshlrev_b32_e32 v238, 2, v252
	v_lshlrev_b32_e32 v252, 4, v252
	v_add_u32_e32 v239, 0x800, v238
	v_add_u32_e32 v240, 0x1000, v238
	v_add_u32_e32 v241, 0x1800, v238
	v_readlane_b32 s86, v254, 4
	v_readlane_b32 s87, v255, 40
	v_readfirstlane_b32 s88, v253
	s_nop 3
	s_lshl_b32 s71, s86, 3
	s_lshl_b32 s87, s87, 3
	s_add_u32 s87, s87, s88
	s_add_u32 s70, s87, 0x26000
	s_mov_b32 s80, 0
	s_mov_b32 s82, 0
	s_mov_b32 s90, 0
	s_waitcnt lgkmcnt(0)
	v_writelane_b32 v254, s3, 39
	s_cmp_lt_i32 s2, s15
	s_nop 0
	v_readfirstlane_b32 s33, v2
	s_cbranch_scc0 .LBB0_1166
	v_ashrrev_i32_e32 v1, 31, v2
	v_lshrrev_b32_e32 v1, 26, v1
	v_add_u32_e32 v1, v2, v1
	v_ashrrev_i32_e32 v4, 6, v1
	v_bfe_i32 v1, v2, 27, 1
	v_lshlrev_b32_e32 v3, 4, v2
	v_lshrrev_b32_e32 v1, 22, v1
	v_add_u32_e32 v1, v3, v1
	v_and_b32_e32 v1, 0xfffffc00, v1
	v_sub_u32_e32 v1, v3, v1
	v_lshrrev_b32_e32 v5, 4, v1
	v_bitop3_b32 v5, v5, v1, 32 bitop3:0x6c
	v_ashrrev_i32_e32 v1, 31, v1
	v_lshrrev_b32_e32 v1, 26, v1
	v_lshlrev_b32_e32 v6, 3, v4
	v_add_u32_e32 v1, v5, v1
	v_and_b32_e32 v6, -16, v6
	v_ashrrev_i32_e32 v7, 6, v1
	v_add_u32_e32 v3, 0x2000, v3
	v_add_u32_e32 v1, v7, v6
	v_ashrrev_i32_e32 v6, 31, v3
	v_lshrrev_b32_e32 v6, 22, v6
	v_add_u32_e32 v6, v3, v6
	s_load_dwordx2 s[0:1], s[0:1], 0x118
	v_ashrrev_i32_e32 v6, 10, v6
	v_mul_i32_i24_e32 v8, 0x400, v6
	v_sub_u32_e32 v3, v3, v8
	v_lshrrev_b32_e32 v8, 4, v3
	v_bitop3_b32 v3, v8, v3, 32 bitop3:0x6c
	s_waitcnt lgkmcnt(0)
	s_add_u32 s2, s0, 0x3ee90000
	v_ashrrev_i32_e32 v9, 31, v3
	s_addc_u32 s3, s1, 0
	v_lshrrev_b32_e32 v9, 26, v9
	s_add_u32 s46, s0, 0x24830000
	v_add_u32_e32 v9, v3, v9
	s_addc_u32 s47, s1, 0
	s_ashr_i32 s11, s33, 6
	v_lshlrev_b32_e32 v8, 3, v6
	v_ashrrev_i32_e32 v10, 6, v9
	v_readlane_b32 s4, v254, 39
	v_and_b32_e32 v9, 0xc0, v9
	s_ashr_i32 s10, s33, 8
	v_and_b32_e32 v8, -16, v8
	s_lshl_b32 s48, s11, 10
	s_lshl_b32 s4, s4, 12
	v_lshlrev_b32_e32 v6, 5, v6
	v_sub_u32_e32 v3, v3, v9
	v_mov_b32_e32 v9, 1
	v_add_u32_e32 v146, v10, v8
	s_add_u32 s8, s46, s4
	v_readlane_b32 s4, v254, 5
	v_and_b32_e32 v6, 32, v6
	v_ashrrev_i16_sdwa v3, v9, sext(v3) dst_sel:DWORD dst_unused:UNUSED_PAD src0_sel:DWORD src1_sel:BYTE_0
	s_addc_u32 s9, s47, 0
	s_ashr_i32 s12, s4, 3
	v_and_b32_e32 v8, 3, v10
	s_mov_b32 s5, 0xfffffe0
	v_lshlrev_b32_e32 v10, 1, v146
	v_lshrrev_b32_e32 v11, 2, v146
	v_add_u32_sdwa v3, v6, sext(v3) dst_sel:DWORD dst_unused:UNUSED_PAD src0_sel:DWORD src1_sel:WORD_0
	s_lshl_b32 s4, s12, 2
	v_and_or_b32 v8, v146, s5, v8
	v_and_b32_e32 v10, 24, v10
	v_and_b32_e32 v11, 4, v11
	v_lshlrev_b32_e32 v6, 8, v3
	s_add_i32 s4, s4, 0
	v_or3_b32 v8, v8, v10, v11
	v_and_b32_e32 v6, 0xffff800, v6
	s_add_i32 s4, s4, 0x21160
	v_add_lshl_u32 v130, v8, v6, 4
	v_and_b32_e32 v6, 3, v7
	v_mul_i32_i24_e32 v7, 64, v7
	v_sub_u32_e32 v5, v5, v7
	v_mov_b32_e32 v7, s4
	ds_read_b32 v7, v7
	v_lshlrev_b32_e32 v8, 1, v1
	v_lshrrev_b32_e32 v10, 2, v1
	v_and_or_b32 v6, v1, s5, v6
	v_and_b32_e32 v8, 24, v8
	v_and_b32_e32 v10, 4, v10
	v_or3_b32 v6, v6, v8, v10
	s_waitcnt lgkmcnt(0)
	v_lshlrev_b32_e32 v8, 2, v7
	v_add_u32_e32 v8, 0, v8
	v_add_u32_e32 v8, 0x21040, v8
	ds_read_b32 v8, v8
	s_lshl_b32 s13, s12, 8
	v_readfirstlane_b32 s4, v7
	s_ashr_i32 s5, s4, 31
	v_lshlrev_b32_e32 v4, 5, v4
	s_waitcnt lgkmcnt(0)
	v_readfirstlane_b32 s14, v8
	s_sub_i32 s12, s12, s14
	s_lshl_b32 s12, s12, 8
	v_cmp_lt_i64_e64 s[6:7], s[4:5], 64
	s_add_i32 s12, s12, 0xff00
	v_and_b32_e32 v4, 32, v4
	v_ashrrev_i16_sdwa v5, v9, sext(v5) dst_sel:DWORD dst_unused:UNUSED_PAD src0_sel:DWORD src1_sel:BYTE_0
	s_and_b64 s[6:7], s[6:7], exec
	v_add_u32_sdwa v4, v4, sext(v5) dst_sel:DWORD dst_unused:UNUSED_PAD src0_sel:DWORD src1_sel:WORD_0
	s_cselect_b32 s12, s13, s12
	s_lshl_b64 s[4:5], s[4:5], 21
	v_lshlrev_b32_e32 v5, 8, v4
	s_add_u32 s38, s8, s4
	v_and_b32_e32 v5, 0xffff800, v5
	s_addc_u32 s39, s9, s5
	s_add_i32 s49, s48, 0
	v_add_lshl_u32 v132, v6, v5, 4
	s_add_i32 m0, s49, 0x10000
	v_add_u32_e32 v5, s12, v1
	v_lshlrev_b32_e32 v149, 1, v4
	v_mov_b32_e32 v135, 0
	global_load_lds_dwordx4 v132, s[38:39]
	s_add_i32 m0, s49, 0x12000
	v_add_u32_e32 v6, s12, v146
	v_add_u32_e32 v147, 0x80, v1
	v_lshl_add_u32 v134, v5, 10, v149
	v_lshlrev_b32_e32 v150, 1, v3
	v_mov_b32_e32 v133, v135
	global_load_lds_dwordx4 v130, s[38:39]
	s_mov_b32 m0, s49
	s_add_i32 s50, s49, 0x2000
	v_add_u32_e32 v7, s12, v147
	v_lshl_add_u32 v136, v6, 10, v150
	v_lshl_add_u64 v[4:5], s[38:39], 0, v[132:133]
	v_mov_b32_e32 v131, v135
	global_load_lds_dwordx4 v134, s[2:3]
	s_mov_b32 m0, s50
	s_mov_b64 s[4:5], 0x800
	v_lshl_add_u32 v138, v7, 10, v149
	v_lshl_add_u64 v[6:7], s[38:39], 0, v[130:131]
	global_load_lds_dwordx4 v136, s[2:3]
	v_lshl_add_u64 v[4:5], v[4:5], 0, s[4:5]
	s_add_i32 m0, s49, 0x14000
	v_add_u32_e32 v148, 0x80, v146
	global_load_lds_dwordx4 v[4:5], off
	v_lshl_add_u64 v[4:5], v[6:7], 0, s[4:5]
	s_add_i32 m0, s49, 0x16000
	s_add_i32 s51, s49, 0x4000
	v_add_u32_e32 v8, s12, v148
	global_load_lds_dwordx4 v[4:5], off
	s_mov_b32 m0, s51
	s_add_i32 s52, s49, 0x6000
	v_lshl_add_u32 v140, v8, 10, v150
	global_load_lds_dwordx4 v138, s[2:3]
	s_mov_b32 m0, s52
	s_mov_b32 s53, 0
	global_load_lds_dwordx4 v140, s[2:3]
	s_mov_b32 s54, 0x10000
	s_cmp_lg_u32 s10, 1
	v_mov_b32_e32 v137, v135
	s_cbranch_scc1 .LBB0_1155
	s_barrier

; __device__ __forceinline__ int tid_fresh() { int t = threadIdx.x; asm volatile("" : "+v"(t)); return t; }
; #define PG8_STAGE(bufoff, gbase, v0, v1) do { \
;         __builtin_amdgcn_global_load_lds((const unsigned*)((const char*)(gbase) + (v0)), (LAS unsigned*)(lds + (bufoff) + ldsw), 16, 0, 0); \
;         __builtin_amdgcn_global_load_lds((const unsigned*)((const char*)(gbase) + (v1)), (LAS unsigned*)(lds + (bufoff) + ldsw + 8192), 16, 0, 0); } while (0)
; template <class Epi, class Sched>
; __device__ __forceinline__ void gemm_phase(LAS unsigned char* lds, const int K, const Sched& S, const Epi& E) {
;     const int tid = tid_fresh(), wid = __builtin_amdgcn_readfirstlane(tid >> 6), lane = tid & 63, wr = wid >> 2, wc = wid & 3, fr = lane & 15, fq = lane >> 4;
;     const int nt = K / BK;
;     int R0, C0, R1, C1; stage_rc(tid * 16, R0, C0); stage_rc(tid * 16 + 8192, R1, C1);
;     const int Rb0 = Epi::PERM ? ((R0 & ~31) + perm32(R0 & 31)) : R0, Rb1 = Epi::PERM ? ((R1 & ~31) + perm32(R1 & 31)) : R1;
;     const unsigned voffB0 = S.b_off(Rb0, C0), voffB1 = S.b_off(Rb1, C1);
;     const size_t kstep = (size_t)(BK * 2);
;     const size_t kstepB = S.b_kstep(), hstep = S.b_hstep();
;     const unsigned ldsw = (unsigned)wid * 1024u;
;     const int aoff = lds_byte(wr * 64 + fr, fq * 8), boff = lds_byte(wc * 32 + fr, fq * 8);
;     ...
;     Unit cur, nxt; int ui = 0;
;     if (!S.next(0, cur)) return;
;     f32x4 acc[2][2][4][2];
; #pragma unroll
;     for (int a = 0; a < 2; ++a)
; #pragma unroll
;         for (int b = 0; b < 2; ++b)
; #pragma unroll
;             for (int m = 0; m < 4; ++m)
; #pragma unroll
;                 for (int n = 0; n < 2; ++n) acc[a][b][m][n] = (f32x4){0.f, 0.f, 0.f, 0.f};
;     bf16x8 At[4][2], B0[2][2], B1[2][2];
;     const char* const gA = S.a_base();
;     unsigned c00, c01, c10, c11, n00, n01, n10, n11;
;     PG8_AOFFS(cur, c00, c01, c10, c11);
;     const char* cB = S.b_ptr(cur);
;     PG8_STAGE(PG8_SB(0, 0), cB, voffB0, voffB1); PG8_STAGE(PG8_SA(0, 0), gA, c00, c01); PG8_STAGE(PG8_SB(0, 1), cB + hstep, voffB0, voffB1); PG8_STAGE(PG8_SA(0, 1), gA, c10, c11);
;     if (wr == 1) PG8_BAR;
;     PG8_WAIT_V(4); PG8_BAR;
;     PG8_STAGE(PG8_SB(1, 0), cB + kstepB, voffB0, voffB1); PG8_STAGE(PG8_SA(1, 0), gA + kstep, c00, c01); PG8_STAGE(PG8_SB(1, 1), cB + hstep + kstepB, voffB0, voffB1);
;     PG8_WAIT_V(6); PG8_BAR;
.LBB0_1281:
	s_or_b64 exec, exec, s[0:1]
	v_readlane_b32 s0, v254, 0
	v_readlane_b32 s2, v254, 17
	v_readlane_b32 s1, v254, 1
	v_mov_b32_e32 v6, v0
	v_readlane_b32 s3, v254, 18
	s_waitcnt lgkmcnt(0)
	s_barrier
	v_readlane_b32 s84, v254, 0
	v_readlane_b32 s85, v254, 1
	s_nop 1
	s_load_dwordx2 s[74:75], s[84:85], 0xd8
	s_load_dwordx2 s[76:77], s[84:85], 0xe0
	s_load_dwordx2 s[78:79], s[84:85], 0x118
	v_and_b32_e32 v252, 63, v0
	v_lshrrev_b32_e32 v253, 6, v0
	v_lshlrev_b32_e32 v238, 2, v252
	v_lshlrev_b32_e32 v252, 4, v252
	v_add_u32_e32 v239, 0x800, v238
	v_add_u32_e32 v240, 0x1000, v238
	v_add_u32_e32 v241, 0x1800, v238
	v_readlane_b32 s86, v254, 4
	v_readlane_b32 s87, v255, 40
	v_readfirstlane_b32 s88, v253
	s_nop 3
	s_lshl_b32 s71, s86, 3
	s_lshl_b32 s87, s87, 3
	s_add_u32 s87, s87, s88
	s_add_u32 s70, s87, 0x20000
	s_mov_b32 s80, 0
	s_mov_b32 s82, 0
	s_mov_b32 s90, 0
	s_waitcnt lgkmcnt(0)
	s_and_b64 vcc, exec, s[2:3]
	v_readfirstlane_b32 s24, v6
	s_cbranch_vccz .LBB0_1295
	v_ashrrev_i32_e32 v1, 31, v6
	v_lshrrev_b32_e32 v1, 26, v1
	v_add_u32_e32 v1, v6, v1
	v_ashrrev_i32_e32 v3, 6, v1
	v_bfe_i32 v1, v6, 27, 1
	v_lshlrev_b32_e32 v2, 4, v6
	v_lshrrev_b32_e32 v1, 22, v1
	v_add_u32_e32 v1, v2, v1
	v_and_b32_e32 v1, 0xfffffc00, v1
	v_sub_u32_e32 v1, v2, v1
	v_lshrrev_b32_e32 v4, 4, v1
	v_bitop3_b32 v4, v4, v1, 32 bitop3:0x6c
	v_ashrrev_i32_e32 v1, 31, v1
	v_lshrrev_b32_e32 v1, 26, v1
	v_lshlrev_b32_e32 v5, 3, v3
	v_add_u32_e32 v1, v4, v1
	v_and_b32_e32 v5, -16, v5
	v_ashrrev_i32_e32 v7, 6, v1
	v_add_u32_e32 v2, 0x2000, v2
	v_add_u32_e32 v1, v7, v5
	v_ashrrev_i32_e32 v5, 31, v2
	v_lshrrev_b32_e32 v5, 22, v5
	v_add_u32_e32 v5, v2, v5
	v_ashrrev_i32_e32 v5, 10, v5
	v_mul_i32_i24_e32 v8, 0x400, v5
	v_sub_u32_e32 v2, v2, v8
	v_lshrrev_b32_e32 v8, 4, v2
	v_bitop3_b32 v2, v8, v2, 32 bitop3:0x6c
	v_ashrrev_i32_e32 v9, 31, v2
	s_load_dwordx2 s[4:5], s[0:1], 0x118
	v_lshrrev_b32_e32 v9, 26, v9
	v_add_u32_e32 v9, v2, v9
	v_ashrrev_i32_e32 v10, 6, v9
	v_and_b32_e32 v9, 0xc0, v9
	v_sub_u32_e32 v2, v2, v9
	v_mov_b32_e32 v9, 1
	v_lshlrev_b32_e32 v8, 3, v5
	v_lshlrev_b32_e32 v5, 5, v5
	v_ashrrev_i16_sdwa v2, v9, sext(v2) dst_sel:DWORD dst_unused:UNUSED_PAD src0_sel:DWORD src1_sel:BYTE_0
	s_waitcnt lgkmcnt(0)
	s_add_u32 s6, s4, 0x34c30000
	v_and_b32_e32 v8, -16, v8
	v_and_b32_e32 v5, 32, v5
	v_bfe_i32 v2, v2, 0, 16
	s_addc_u32 s7, s5, 0
	v_add_u32_e32 v150, v10, v8
	v_and_b32_e32 v8, 3, v10
	s_mov_b32 s0, 0xfffe0
	v_add_lshl_u32 v151, v5, v2, 1
	v_and_b32_e32 v2, 3, v7
	s_add_u32 s25, s4, 0x2030000
	v_and_or_b32 v8, v150, s0, v8
	v_and_or_b32 v2, v1, s0, v2
	v_readlane_b32 s0, v254, 15
	s_addc_u32 s26, s5, 0
	s_lshr_b32 s0, s0, 29
	v_readlane_b32 s10, v254, 5
	s_add_i32 s0, s10, s0
	s_ashr_i32 s2, s24, 6
	s_ashr_i32 s3, s0, 3
	s_and_b32 s0, s0, -8
	s_ashr_i32 s1, s24, 8
	s_lshl_b32 s27, s2, 10
	s_sub_i32 s0, s10, s0
	s_cmp_lt_i32 s0, 0
	s_movk_i32 s28, 0x61
	s_cselect_b32 s10, s28, 0x60
	s_mul_i32 s0, s10, s0
	s_add_i32 s0, s0, s3
	s_mul_hi_i32 s3, s0, 0x2aaaaaab
	s_lshr_b32 s10, s3, 31
	s_ashr_i32 s3, s3, 5
	s_add_i32 s3, s3, s10
	s_mul_i32 s10, s3, 0xc0
	s_sub_i32 s10, s0, s10
	v_lshrrev_b32_e32 v10, 2, v150
	v_lshlrev_b32_e32 v11, 1, v150
	s_bfe_u32 s0, s10, 0x3001c
	v_and_b32_e32 v10, 4, v10
	v_and_b32_e32 v11, 24, v11
	s_add_i32 s11, s10, s0
	v_or3_b32 v8, v8, v10, v11
	s_sext_i32_i16 s0, s11
	s_and_b32 s11, s11, 0xfff8
	v_lshl_add_u32 v130, v8, 12, v151
	v_lshrrev_b32_e32 v5, 2, v1
	v_lshlrev_b32_e32 v8, 1, v1
	s_sub_i32 s10, s10, s11
	v_and_b32_e32 v5, 4, v5
	v_and_b32_e32 v8, 24, v8
	s_sext_i32_i16 s10, s10
	v_or3_b32 v2, v2, v5, v8
	v_mul_i32_i24_e32 v5, 64, v7
	s_lshr_b32 s0, s0, 3
	s_lshl_b32 s3, s3, 11
	s_lshl_b32 s10, s10, 8
	v_sub_u32_e32 v4, v4, v5
	s_add_i32 s43, s10, s3
	s_bfe_i64 s[10:11], s[0:1], 0x100000
	v_lshlrev_b32_e32 v3, 5, v3
	v_ashrrev_i16_sdwa v4, v9, sext(v4) dst_sel:DWORD dst_unused:UNUSED_PAD src0_sel:DWORD src1_sel:BYTE_0
	s_lshl_b64 s[10:11], s[10:11], 20
	v_and_b32_e32 v3, 32, v3
	v_bfe_i32 v4, v4, 0, 16
	s_add_u32 s18, s25, s10
	v_add_lshl_u32 v152, v3, v4, 1
	s_addc_u32 s19, s26, s11
	s_add_i32 s29, s27, 0
	v_lshl_add_u32 v132, v2, 12, v152
	s_add_i32 m0, s29, 0x10000
	v_add_u32_e32 v2, s43, v1
	global_load_lds_dwordx4 v132, s[18:19]
	s_add_i32 m0, s29, 0x12000
	v_add_u32_e32 v3, s43, v150
	v_lshl_add_u32 v134, v2, 12, v152
	global_load_lds_dwordx4 v130, s[18:19]
	s_mov_b32 m0, s29
	s_add_i32 s30, s29, 0x2000
	v_lshl_add_u32 v140, v3, 12, v151
	global_load_lds_dwordx4 v134, s[6:7]
	s_mov_b32 m0, s30
	s_add_u32 s10, s18, 0x80000
	v_add_u32_e32 v153, 0x80, v1
	global_load_lds_dwordx4 v140, s[6:7]
	s_addc_u32 s11, s19, 0
	s_add_i32 m0, s29, 0x14000
	v_add_u32_e32 v4, s43, v153
	v_add_u32_e32 v154, 0x80, v150
	global_load_lds_dwordx4 v132, s[10:11]
	s_add_i32 m0, s29, 0x16000
	s_add_i32 s31, s29, 0x4000
	v_add_u32_e32 v5, s43, v154
	v_lshl_add_u32 v142, v4, 12, v152
	global_load_lds_dwordx4 v130, s[10:11]
	s_mov_b32 m0, s31
	s_add_i32 s33, s29, 0x6000
	v_lshl_add_u32 v144, v5, 12, v151
	global_load_lds_dwordx4 v142, s[6:7]
	s_mov_b32 m0, s33
	v_mov_b32_e32 v135, 0
	global_load_lds_dwordx4 v144, s[6:7]
	v_mov_b32_e32 v133, v135
	v_mov_b32_e32 v131, v135
	s_mov_b32 s34, 0
	v_lshl_add_u64 v[4:5], s[18:19], 0, v[132:133]
	v_lshl_add_u64 v[2:3], s[18:19], 0, v[130:131]
	s_cmp_lg_u32 s1, 1
	v_mov_b32_e32 v141, v135
	s_cbranch_scc1 .LBB0_1284
	s_barrier

; #define PG8_STAGE(bufoff, gbase, v0, v1) do { \
;         __builtin_amdgcn_global_load_lds((const unsigned*)((const char*)(gbase) + (v0)), (LAS unsigned*)(lds + (bufoff) + ldsw), 16, 0, 0); \
;         __builtin_amdgcn_global_load_lds((const unsigned*)((const char*)(gbase) + (v1)), (LAS unsigned*)(lds + (bufoff) + ldsw + 8192), 16, 0, 0); } while (0)
; #define PG8_LDA(dst, b, h) do { _Pragma("unroll") for (int m = 0; m < 4; ++m) _Pragma("unroll") for (int k = 0; k < 2; ++k) dst[m][k] = *(const LAS bf16x8*)(lds + PG8_SA(b, h) + aoff + m * 2048 + k * 1024); } while (0)
; #define PG8_LDB(dst, b, h) do { _Pragma("unroll") for (int n = 0; n < 2; ++n) _Pragma("unroll") for (int k = 0; k < 2; ++k) dst[n][k] = *(const LAS bf16x8*)(lds + PG8_SB(b, h) + boff + n * 2048 + k * 1024); } while (0)
; #define PG8_MMA(ai, bj, At, Bt) do { __builtin_amdgcn_s_setprio(1); _Pragma("unroll") for (int m = 0; m < 4; ++m) _Pragma("unroll") for (int n = 0; n < 2; ++n) _Pragma("unroll") for (int k = 0; k < 2; ++k) \
;         acc[ai][bj][m][n] = __builtin_amdgcn_mfma_f32_16x16x32_bf16(Bt[n][k], At[m][k], acc[ai][bj][m][n], 0, 0, 0); __builtin_amdgcn_s_setprio(0); } while (0)
; #define PG8_WAIT_V(n) asm volatile("s_waitcnt vmcnt(" #n ")" ::: "memory")
; #define PG8_WAIT_L(n) asm volatile("s_waitcnt lgkmcnt(" #n ")" ::: "memory")
; #define PG8_BAR __builtin_amdgcn_s_barrier()
; #define PG8_SCHED __builtin_amdgcn_sched_barrier(0)
; template <class Epi, class Sched>
; __device__ __forceinline__ void gemm_phase(LAS unsigned char* lds, const int K, const Sched& S, const Epi& E) {
;     ...
;             PG8_LDB(B0, 0, 0); PG8_SCHED; PG8_LDA(At, 0, 0); PG8_STAGE(PG8_SA(1, 1), a1, c10, c11);
;             PG8_WAIT_L(8); PG8_BAR; PG8_WAIT_L(0); PG8_MMA(0, 0, At, B0); PG8_BAR; PG8_SCHED;
;             PG8_LDB(B1, 0, 1); PG8_STAGE(PG8_SB(0, 0), b2, voffB0, voffB1);
;             PG8_BAR; PG8_WAIT_L(0); PG8_MMA(0, 1, At, B1); PG8_BAR;
;             PG8_LDA(At, 0, 1); PG8_STAGE(PG8_SA(0, 0), a2, x00, x01);
;             PG8_BAR; PG8_WAIT_L(0); PG8_MMA(1, 0, At, B0); PG8_BAR; PG8_SCHED;
;             PG8_STAGE(PG8_SB(0, 1), b2 + hstep, voffB0, voffB1);
;             PG8_WAIT_V(6); PG8_BAR; PG8_MMA(1, 1, At, B1); PG8_BAR;
.LBB0_1290:
	s_add_u32 s20, s4, s18
	s_addc_u32 s21, s5, s19
	s_add_u32 s22, s20, 0x34c30100
	ds_read_b128 v[166:169], v158
	ds_read_b128 v[170:173], v158 offset:1024
	ds_read_b128 v[174:177], v158 offset:2048
	ds_read_b128 v[178:181], v158 offset:3072
	s_addc_u32 s23, s21, 0
	s_add_u32 s47, s17, s18
	s_addc_u32 s48, s45, s19
	s_cmpk_eq_i32 s18, 0xf00
	s_cselect_b64 vcc, -1, 0
	s_and_b64 s[20:21], vcc, exec
	v_cndmask_b32_e32 v134, v141, v161, vcc
	s_cselect_b32 s23, s7, s23
	s_cselect_b32 s22, s6, s22
	v_cndmask_b32_e32 v143, v142, v163, vcc
	s_cselect_b32 s21, s3, s48
	s_cselect_b32 s20, s2, s47
	v_cndmask_b32_e32 v206, v140, v162, vcc
	s_mov_b32 m0, s40
	v_lshl_add_u64 v[216:217], v[148:149], 0, s[18:19]
	ds_read_b128 v[182:185], v159
	ds_read_b128 v[186:189], v159 offset:1024
	ds_read_b128 v[190:193], v159 offset:2048
	ds_read_b128 v[194:197], v159 offset:3072
	ds_read_b128 v[198:201], v159 offset:4096
	ds_read_b128 v[202:205], v159 offset:5120
	ds_read_b128 v[208:211], v159 offset:6144
	ds_read_b128 v[212:215], v159 offset:7168
	global_load_lds_dwordx4 v[216:217], off
	v_lshl_add_u64 v[216:217], v[146:147], 0, s[18:19]
	s_add_i32 m0, s29, 0xe000
	s_nop 0
	global_load_lds_dwordx4 v[216:217], off
	s_waitcnt lgkmcnt(8)
	s_barrier
	s_waitcnt lgkmcnt(0)
	s_setprio 1
	s_waitcnt lgkmcnt(0)
	v_mfma_f32_16x16x32_bf16 v[126:129], v[166:169], v[182:185], v[126:129]
	v_mfma_f32_16x16x32_bf16 v[122:125], v[174:177], v[182:185], v[122:125]
	v_mfma_f32_16x16x32_bf16 v[118:121], v[166:169], v[190:193], v[118:121]
	v_mfma_f32_16x16x32_bf16 v[110:113], v[174:177], v[190:193], v[110:113]
	v_mfma_f32_16x16x32_bf16 v[102:105], v[166:169], v[198:201], v[102:105]
	v_mfma_f32_16x16x32_bf16 v[94:97], v[174:177], v[198:201], v[94:97]
	v_mfma_f32_16x16x32_bf16 v[86:89], v[166:169], v[208:211], v[86:89]
	v_mfma_f32_16x16x32_bf16 v[78:81], v[174:177], v[208:211], v[78:81]
	v_mfma_f32_16x16x32_bf16 v[126:129], v[170:173], v[186:189], v[126:129]
	v_mfma_f32_16x16x32_bf16 v[122:125], v[178:181], v[186:189], v[122:125]
	v_mfma_f32_16x16x32_bf16 v[118:121], v[170:173], v[194:197], v[118:121]
	v_mfma_f32_16x16x32_bf16 v[110:113], v[178:181], v[194:197], v[110:113]
	v_mfma_f32_16x16x32_bf16 v[102:105], v[170:173], v[202:205], v[102:105]
	v_mfma_f32_16x16x32_bf16 v[94:97], v[178:181], v[202:205], v[94:97]
	v_mfma_f32_16x16x32_bf16 v[86:89], v[170:173], v[212:215], v[86:89]
	v_mfma_f32_16x16x32_bf16 v[78:81], v[178:181], v[212:215], v[78:81]
	s_setprio 0
	s_barrier
	s_add_i32 s47, s37, s27
	v_lshl_add_u64 v[232:233], s[20:21], 0, v[132:133]
	s_mov_b32 m0, s47
	ds_read_b128 v[216:219], v160
	ds_read_b128 v[220:223], v160 offset:1024
	ds_read_b128 v[224:227], v160 offset:2048
	ds_read_b128 v[228:231], v160 offset:3072
	global_load_lds_dwordx4 v[232:233], off
	v_lshl_add_u64 v[234:235], s[20:21], 0, v[130:131]
	s_add_i32 m0, s47, 0x2000
	s_nop 0
	global_load_lds_dwordx4 v[234:235], off
	s_barrier
	s_waitcnt lgkmcnt(0)
	s_setprio 1
	s_waitcnt lgkmcnt(0)
	v_mfma_f32_16x16x32_bf16 v[114:117], v[216:219], v[182:185], v[114:117]
	v_mfma_f32_16x16x32_bf16 v[106:109], v[224:227], v[182:185], v[106:109]
	v_mfma_f32_16x16x32_bf16 v[98:101], v[216:219], v[190:193], v[98:101]
	v_mfma_f32_16x16x32_bf16 v[90:93], v[224:227], v[190:193], v[90:93]
	v_mfma_f32_16x16x32_bf16 v[82:85], v[216:219], v[198:201], v[82:85]
	v_mfma_f32_16x16x32_bf16 v[74:77], v[224:227], v[198:201], v[74:77]
	v_mfma_f32_16x16x32_bf16 v[70:73], v[216:219], v[208:211], v[70:73]
	v_mfma_f32_16x16x32_bf16 v[66:69], v[224:227], v[208:211], v[66:69]
	v_mfma_f32_16x16x32_bf16 v[114:117], v[220:223], v[186:189], v[114:117]
	v_mfma_f32_16x16x32_bf16 v[106:109], v[228:231], v[186:189], v[106:109]
	v_mfma_f32_16x16x32_bf16 v[98:101], v[220:223], v[194:197], v[98:101]
	v_mfma_f32_16x16x32_bf16 v[90:93], v[228:231], v[194:197], v[90:93]
	v_mfma_f32_16x16x32_bf16 v[82:85], v[220:223], v[202:205], v[82:85]
	v_mfma_f32_16x16x32_bf16 v[74:77], v[228:231], v[202:205], v[74:77]
	v_mfma_f32_16x16x32_bf16 v[70:73], v[220:223], v[212:215], v[70:73]
	v_mfma_f32_16x16x32_bf16 v[66:69], v[228:231], v[212:215], v[66:69]
	s_setprio 0
	s_mov_b32 m0, s29
	s_barrier
	ds_read_b128 v[182:185], v159 offset:16384
	ds_read_b128 v[186:189], v159 offset:17408
	ds_read_b128 v[190:193], v159 offset:18432
	ds_read_b128 v[194:197], v159 offset:19456
	ds_read_b128 v[198:201], v159 offset:20480
	ds_read_b128 v[202:205], v159 offset:21504
	ds_read_b128 v[208:211], v159 offset:22528
	ds_read_b128 v[212:215], v159 offset:23552
	global_load_lds_dwordx4 v134, s[22:23]
	s_mov_b32 m0, s30
	v_mov_b32_e32 v207, v135
	global_load_lds_dwordx4 v206, s[22:23]
	s_barrier
	s_waitcnt lgkmcnt(0)
	v_lshl_add_u64 v[236:237], s[22:23], 0, v[134:135]
	v_lshl_add_u64 v[206:207], s[22:23], 0, v[206:207]
	s_setprio 1
	s_waitcnt lgkmcnt(0)
	v_mfma_f32_16x16x32_bf16 v[62:65], v[166:169], v[182:185], v[62:65]
	v_mfma_f32_16x16x32_bf16 v[58:61], v[174:177], v[182:185], v[58:61]
	v_mfma_f32_16x16x32_bf16 v[54:57], v[166:169], v[190:193], v[54:57]
	v_mfma_f32_16x16x32_bf16 v[46:49], v[174:177], v[190:193], v[46:49]
	v_mfma_f32_16x16x32_bf16 v[38:41], v[166:169], v[198:201], v[38:41]
	v_mfma_f32_16x16x32_bf16 v[30:33], v[174:177], v[198:201], v[30:33]
	v_mfma_f32_16x16x32_bf16 v[22:25], v[166:169], v[208:211], v[22:25]
	v_mfma_f32_16x16x32_bf16 v[14:17], v[174:177], v[208:211], v[14:17]
	v_mfma_f32_16x16x32_bf16 v[62:65], v[170:173], v[186:189], v[62:65]
	v_mfma_f32_16x16x32_bf16 v[58:61], v[178:181], v[186:189], v[58:61]
	v_mfma_f32_16x16x32_bf16 v[54:57], v[170:173], v[194:197], v[54:57]
	v_mfma_f32_16x16x32_bf16 v[46:49], v[178:181], v[194:197], v[46:49]
	v_mfma_f32_16x16x32_bf16 v[38:41], v[170:173], v[202:205], v[38:41]
	v_mfma_f32_16x16x32_bf16 v[30:33], v[178:181], v[202:205], v[30:33]
	v_mfma_f32_16x16x32_bf16 v[22:25], v[170:173], v[212:215], v[22:25]
	v_mfma_f32_16x16x32_bf16 v[14:17], v[178:181], v[212:215], v[14:17]
	s_setprio 0
	s_barrier
	s_add_u32 s48, s20, 0x80000
	s_addc_u32 s49, s21, 0
	s_add_i32 s47, s38, s27
	v_lshl_add_u64 v[166:167], s[48:49], 0, v[132:133]
	s_mov_b32 m0, s47
	s_nop 0
	global_load_lds_dwordx4 v[166:167], off
	v_lshl_add_u64 v[166:167], s[48:49], 0, v[130:131]
	s_add_i32 m0, s47, 0x2000
	s_nop 0
	global_load_lds_dwordx4 v[166:167], off
	s_cmp_eq_u32 s82, 0
	s_cbranch_scc1 .Lpb11_p4n
	s_waitcnt vmcnt(14)
	v_cvt_pk_bf16_f32 v244, v244, v245
	v_cvt_pk_bf16_f32 v245, v246, v247
	v_cvt_pk_bf16_f32 v246, v248, v249
	v_cvt_pk_bf16_f32 v247, v250, v251
	global_store_dwordx4 v253, v[244:247], s[78:79] nt
	s_mov_b32 s82, 0
	s_waitcnt vmcnt(7)
	s_branch .Lpb11_p4j

; #define PG8_STAGE(bufoff, gbase, v0, v1) do { \
;         __builtin_amdgcn_global_load_lds((const unsigned*)((const char*)(gbase) + (v0)), (LAS unsigned*)(lds + (bufoff) + ldsw), 16, 0, 0); \
;         __builtin_amdgcn_global_load_lds((const unsigned*)((const char*)(gbase) + (v1)), (LAS unsigned*)(lds + (bufoff) + ldsw + 8192), 16, 0, 0); } while (0)
; #define PG8_LDA(dst, b, h) do { _Pragma("unroll") for (int m = 0; m < 4; ++m) _Pragma("unroll") for (int k = 0; k < 2; ++k) dst[m][k] = *(const LAS bf16x8*)(lds + PG8_SA(b, h) + aoff + m * 2048 + k * 1024); } while (0)
; #define PG8_LDB(dst, b, h) do { _Pragma("unroll") for (int n = 0; n < 2; ++n) _Pragma("unroll") for (int k = 0; k < 2; ++k) dst[n][k] = *(const LAS bf16x8*)(lds + PG8_SB(b, h) + boff + n * 2048 + k * 1024); } while (0)
; #define PG8_MMA(ai, bj, At, Bt) do { __builtin_amdgcn_s_setprio(1); _Pragma("unroll") for (int m = 0; m < 4; ++m) _Pragma("unroll") for (int n = 0; n < 2; ++n) _Pragma("unroll") for (int k = 0; k < 2; ++k) \
;         acc[ai][bj][m][n] = __builtin_amdgcn_mfma_f32_16x16x32_bf16(Bt[n][k], At[m][k], acc[ai][bj][m][n], 0, 0, 0); __builtin_amdgcn_s_setprio(0); } while (0)
; #define PG8_WAIT_V(n) asm volatile("s_waitcnt vmcnt(" #n ")" ::: "memory")
; #define PG8_BAR __builtin_amdgcn_s_barrier()
; #define PG8_SCHED __builtin_amdgcn_sched_barrier(0)
; template <class Epi, class Sched>
; __device__ __forceinline__ void gemm_phase(LAS unsigned char* lds, const int K, const Sched& S, const Epi& E) {
;     ...
;             PG8_WAIT_V(6); PG8_BAR; PG8_MMA(1, 1, At, B1); PG8_BAR;
;             PG8_LDB(B0, 1, 0); PG8_SCHED; PG8_LDA(At, 1, 0); PG8_STAGE(PG8_SA(0, 1), a2, x10, x11);
; __device__ __forceinline__ bool bg_decode(int st, int wg, int NW, int lane, KP kp, const float*& src, int& ldS, bf16_t*& dst, int& o2) {
;     ...
;     if (r < 65536) {
;         const int e = r >> 10, kc = (r >> 2) & 255, kind = (r >> 1) & 1, cc = r & 1, n = cc * 256 + lane;
;         ldS = FF; o2 = 256 * 8;
;         src = kp->in[27 + kind] + ((size_t)(l * NE + e) * D + kc * 8) * FF + n;
;         const int drow = (n >> 7) * 256 + kind * 128 + (n & 127);
;         dst = (bf16_t*)(ws + WS_WGU) + l * WGU_L + (size_t)e * 1024 * D + ((size_t)kc * 1024 + drow) * 8;
.Lpb11_p4j:
	s_barrier
	s_setprio 1
	v_mfma_f32_16x16x32_bf16 v[50:53], v[216:219], v[182:185], v[50:53]
	v_mfma_f32_16x16x32_bf16 v[42:45], v[224:227], v[182:185], v[42:45]
	v_mfma_f32_16x16x32_bf16 v[34:37], v[216:219], v[190:193], v[34:37]
	v_mfma_f32_16x16x32_bf16 v[26:29], v[224:227], v[190:193], v[26:29]
	v_mfma_f32_16x16x32_bf16 v[18:21], v[216:219], v[198:201], v[18:21]
	v_mfma_f32_16x16x32_bf16 v[10:13], v[224:227], v[198:201], v[10:13]
	v_mfma_f32_16x16x32_bf16 v[6:9], v[216:219], v[208:211], v[6:9]
	v_mfma_f32_16x16x32_bf16 v[2:5], v[224:227], v[208:211], v[2:5]
	v_mfma_f32_16x16x32_bf16 v[50:53], v[220:223], v[186:189], v[50:53]
	v_mfma_f32_16x16x32_bf16 v[42:45], v[228:231], v[186:189], v[42:45]
	v_mfma_f32_16x16x32_bf16 v[34:37], v[220:223], v[194:197], v[34:37]
	v_mfma_f32_16x16x32_bf16 v[26:29], v[228:231], v[194:197], v[26:29]
	v_mfma_f32_16x16x32_bf16 v[18:21], v[220:223], v[202:205], v[18:21]
	v_mfma_f32_16x16x32_bf16 v[10:13], v[228:231], v[202:205], v[10:13]
	v_mfma_f32_16x16x32_bf16 v[6:9], v[220:223], v[212:215], v[6:9]
	v_mfma_f32_16x16x32_bf16 v[2:5], v[228:231], v[212:215], v[2:5]
	s_setprio 0
	s_add_i32 s47, 0, 0x18000
	v_add_u32_e32 v134, s47, v156
	s_barrier
	ds_read_b128 v[166:169], v134
	ds_read_b128 v[170:173], v134 offset:1024
	ds_read_b128 v[174:177], v134 offset:2048
	ds_read_b128 v[178:181], v134 offset:3072
	s_mov_b32 m0, s31
	ds_read_b128 v[182:185], v159 offset:32768
	ds_read_b128 v[186:189], v159 offset:33792
	ds_read_b128 v[190:193], v159 offset:34816
	ds_read_b128 v[194:197], v159 offset:35840
	ds_read_b128 v[198:201], v159 offset:36864
	ds_read_b128 v[202:205], v159 offset:37888
	ds_read_b128 v[208:211], v159 offset:38912
	ds_read_b128 v[212:215], v159 offset:39936
	v_cndmask_b32_e32 v134, v144, v164, vcc
	global_load_lds_dwordx4 v143, s[22:23]
	s_mov_b32 m0, s33
	s_nop 0
	global_load_lds_dwordx4 v134, s[22:23]
	s_cmp_ge_u32 s70, 0x26000
	s_cbranch_scc1 .Lpb11_p5n
	s_cmp_eq_u32 s80, 0
	s_cbranch_scc0 .Lpb11_adv4
	s_cmp_ge_u32 s70, 0x18000
	s_cselect_b32 s84, 0x18000, 0
	s_cselect_b32 s83, 0x10000000, 0
	s_mov_b32 s81, 0x4030000
	s_cselect_b32 s81, 0x14430000, s81
	s_sub_u32 s84, s70, s84
	s_lshr_b32 s85, s84, 2
	s_lshl_b32 s85, s85, 14
	s_and_b32 s86, s84, 1
	s_lshl_b32 s87, s86, 10
	s_add_u32 s87, s87, s85
	s_add_u32 s87, s87, s83
	s_bitcmp1_b32 s84, 1
	s_cselect_b64 s[72:73], s[76:77], s[74:75]
	s_add_u32 s72, s72, s87
	s_addc_u32 s73, s73, 0
	s_add_u32 s88, s72, 0x2000
	s_addc_u32 s89, s73, 0
	s_lshl_b32 s86, s86, 13
	s_add_u32 s85, s85, s86
	s_and_b32 s86, s84, 2
	s_lshl_b32 s86, s86, 10
	s_add_u32 s85, s85, s86
	s_add_u32 s85, s85, s81
	v_add_u32_e32 v253, s85, v252
	s_movk_i32 s81, 0x400
	s_branch .Lpb11_ld4

; #define PG8_STAGE(bufoff, gbase, v0, v1) do { \
;         __builtin_amdgcn_global_load_lds((const unsigned*)((const char*)(gbase) + (v0)), (LAS unsigned*)(lds + (bufoff) + ldsw), 16, 0, 0); \
;         __builtin_amdgcn_global_load_lds((const unsigned*)((const char*)(gbase) + (v1)), (LAS unsigned*)(lds + (bufoff) + ldsw + 8192), 16, 0, 0); } while (0)
; #define PG8_LDA(dst, b, h) do { _Pragma("unroll") for (int m = 0; m < 4; ++m) _Pragma("unroll") for (int k = 0; k < 2; ++k) dst[m][k] = *(const LAS bf16x8*)(lds + PG8_SA(b, h) + aoff + m * 2048 + k * 1024); } while (0)
; #define PG8_LDB(dst, b, h) do { _Pragma("unroll") for (int n = 0; n < 2; ++n) _Pragma("unroll") for (int k = 0; k < 2; ++k) dst[n][k] = *(const LAS bf16x8*)(lds + PG8_SB(b, h) + boff + n * 2048 + k * 1024); } while (0)
; #define PG8_MMA(ai, bj, At, Bt) do { __builtin_amdgcn_s_setprio(1); _Pragma("unroll") for (int m = 0; m < 4; ++m) _Pragma("unroll") for (int n = 0; n < 2; ++n) _Pragma("unroll") for (int k = 0; k < 2; ++k) \
;         acc[ai][bj][m][n] = __builtin_amdgcn_mfma_f32_16x16x32_bf16(Bt[n][k], At[m][k], acc[ai][bj][m][n], 0, 0, 0); __builtin_amdgcn_s_setprio(0); } while (0)
; #define PG8_WAIT_V(n) asm volatile("s_waitcnt vmcnt(" #n ")" ::: "memory")
; #define PG8_WAIT_L(n) asm volatile("s_waitcnt lgkmcnt(" #n ")" ::: "memory")
; #define PG8_BAR __builtin_amdgcn_s_barrier()
; #define PG8_SCHED __builtin_amdgcn_sched_barrier(0)
; template <class Epi, class Sched>
; __device__ __forceinline__ void gemm_phase(LAS unsigned char* lds, const int K, const Sched& S, const Epi& E) {
;     ...
;             PG8_WAIT_L(8); PG8_BAR; PG8_WAIT_L(0); PG8_MMA(0, 0, At, B0); PG8_BAR; PG8_SCHED;
;             PG8_LDB(B1, 1, 1); PG8_STAGE(PG8_SB(1, 0), b3, voffB0, voffB1);
;             PG8_BAR; PG8_WAIT_L(0); PG8_MMA(0, 1, At, B1); PG8_BAR;
;             PG8_LDA(At, 1, 1); PG8_STAGE(PG8_SA(1, 0), a3, x00, x01);
;             PG8_BAR; PG8_WAIT_L(0); PG8_MMA(1, 0, At, B0); PG8_BAR; PG8_SCHED;
;             PG8_STAGE(PG8_SB(1, 1), b3 + hstep, voffB0, voffB1);
;             PG8_WAIT_V(6); PG8_BAR; PG8_MMA(1, 1, At, B1); PG8_BAR;
.Lpb11_p5n:
	s_waitcnt lgkmcnt(8)
	s_barrier
	s_waitcnt lgkmcnt(0)
	s_setprio 1
	s_waitcnt lgkmcnt(0)
	v_mfma_f32_16x16x32_bf16 v[126:129], v[166:169], v[182:185], v[126:129]
	v_mfma_f32_16x16x32_bf16 v[122:125], v[174:177], v[182:185], v[122:125]
	v_mfma_f32_16x16x32_bf16 v[118:121], v[166:169], v[190:193], v[118:121]
	v_mfma_f32_16x16x32_bf16 v[110:113], v[174:177], v[190:193], v[110:113]
	v_mfma_f32_16x16x32_bf16 v[102:105], v[166:169], v[198:201], v[102:105]
	v_mfma_f32_16x16x32_bf16 v[94:97], v[174:177], v[198:201], v[94:97]
	v_mfma_f32_16x16x32_bf16 v[86:89], v[166:169], v[208:211], v[86:89]
	v_mfma_f32_16x16x32_bf16 v[78:81], v[174:177], v[208:211], v[78:81]
	v_mfma_f32_16x16x32_bf16 v[126:129], v[170:173], v[186:189], v[126:129]
	v_mfma_f32_16x16x32_bf16 v[122:125], v[178:181], v[186:189], v[122:125]
	v_mfma_f32_16x16x32_bf16 v[118:121], v[170:173], v[194:197], v[118:121]
	v_mfma_f32_16x16x32_bf16 v[110:113], v[178:181], v[194:197], v[110:113]
	v_mfma_f32_16x16x32_bf16 v[102:105], v[170:173], v[202:205], v[102:105]
	v_mfma_f32_16x16x32_bf16 v[94:97], v[178:181], v[202:205], v[94:97]
	v_mfma_f32_16x16x32_bf16 v[86:89], v[170:173], v[212:215], v[86:89]
	v_mfma_f32_16x16x32_bf16 v[78:81], v[178:181], v[212:215], v[78:81]
	s_setprio 0
	s_barrier
	s_add_i32 s22, 0, 0x1c000
	s_add_i32 s23, s47, s27
	v_add_u32_e32 v134, s22, v156
	v_lshl_add_u64 v[232:233], v[232:233], 0, s[14:15]
	s_mov_b32 m0, s23
	ds_read_b128 v[216:219], v134
	ds_read_b128 v[220:223], v134 offset:1024
	ds_read_b128 v[224:227], v134 offset:2048
	ds_read_b128 v[228:231], v134 offset:3072
	global_load_lds_dwordx4 v[232:233], off
	v_lshl_add_u64 v[232:233], v[234:235], 0, s[14:15]
	s_add_i32 m0, s23, 0x2000
	s_nop 0
	global_load_lds_dwordx4 v[232:233], off
	s_barrier
	s_waitcnt lgkmcnt(0)
	s_setprio 1
	s_waitcnt lgkmcnt(0)
	v_mfma_f32_16x16x32_bf16 v[114:117], v[216:219], v[182:185], v[114:117]
	v_mfma_f32_16x16x32_bf16 v[106:109], v[224:227], v[182:185], v[106:109]
	v_mfma_f32_16x16x32_bf16 v[98:101], v[216:219], v[190:193], v[98:101]
	v_mfma_f32_16x16x32_bf16 v[90:93], v[224:227], v[190:193], v[90:93]
	v_mfma_f32_16x16x32_bf16 v[82:85], v[216:219], v[198:201], v[82:85]
	v_mfma_f32_16x16x32_bf16 v[74:77], v[224:227], v[198:201], v[74:77]
	v_mfma_f32_16x16x32_bf16 v[70:73], v[216:219], v[208:211], v[70:73]
	v_mfma_f32_16x16x32_bf16 v[66:69], v[224:227], v[208:211], v[66:69]
	v_mfma_f32_16x16x32_bf16 v[114:117], v[220:223], v[186:189], v[114:117]
	v_mfma_f32_16x16x32_bf16 v[106:109], v[228:231], v[186:189], v[106:109]
	v_mfma_f32_16x16x32_bf16 v[98:101], v[220:223], v[194:197], v[98:101]
	v_mfma_f32_16x16x32_bf16 v[90:93], v[228:231], v[194:197], v[90:93]
	v_mfma_f32_16x16x32_bf16 v[82:85], v[220:223], v[202:205], v[82:85]
	v_mfma_f32_16x16x32_bf16 v[74:77], v[228:231], v[202:205], v[74:77]
	v_mfma_f32_16x16x32_bf16 v[70:73], v[220:223], v[212:215], v[70:73]
	v_mfma_f32_16x16x32_bf16 v[66:69], v[228:231], v[212:215], v[66:69]
	s_setprio 0
	s_mov_b32 m0, s35
	v_lshl_add_u64 v[232:233], v[236:237], 0, s[14:15]
	s_barrier
	ds_read_b128 v[182:185], v159 offset:49152
	ds_read_b128 v[186:189], v159 offset:50176
	ds_read_b128 v[190:193], v159 offset:51200
	ds_read_b128 v[194:197], v159 offset:52224
	ds_read_b128 v[198:201], v159 offset:53248
	ds_read_b128 v[202:205], v159 offset:54272
	ds_read_b128 v[208:211], v159 offset:55296
	ds_read_b128 v[212:215], v159 offset:56320
	global_load_lds_dwordx4 v[232:233], off
	v_lshl_add_u64 v[206:207], v[206:207], 0, s[14:15]
	s_mov_b32 m0, s36
	s_nop 0
	global_load_lds_dwordx4 v[206:207], off
	s_barrier
	s_waitcnt lgkmcnt(0)
	s_setprio 1
	s_waitcnt lgkmcnt(0)
	v_mfma_f32_16x16x32_bf16 v[62:65], v[166:169], v[182:185], v[62:65]
	v_mfma_f32_16x16x32_bf16 v[58:61], v[174:177], v[182:185], v[58:61]
	v_mfma_f32_16x16x32_bf16 v[54:57], v[166:169], v[190:193], v[54:57]
	v_mfma_f32_16x16x32_bf16 v[46:49], v[174:177], v[190:193], v[46:49]
	v_mfma_f32_16x16x32_bf16 v[38:41], v[166:169], v[198:201], v[38:41]
	v_mfma_f32_16x16x32_bf16 v[30:33], v[174:177], v[198:201], v[30:33]
	v_mfma_f32_16x16x32_bf16 v[22:25], v[166:169], v[208:211], v[22:25]
	v_mfma_f32_16x16x32_bf16 v[14:17], v[174:177], v[208:211], v[14:17]
	v_mfma_f32_16x16x32_bf16 v[62:65], v[170:173], v[186:189], v[62:65]
	v_mfma_f32_16x16x32_bf16 v[58:61], v[178:181], v[186:189], v[58:61]
	v_mfma_f32_16x16x32_bf16 v[54:57], v[170:173], v[194:197], v[54:57]
	v_mfma_f32_16x16x32_bf16 v[46:49], v[178:181], v[194:197], v[46:49]
	v_mfma_f32_16x16x32_bf16 v[38:41], v[170:173], v[202:205], v[38:41]
	v_mfma_f32_16x16x32_bf16 v[30:33], v[178:181], v[202:205], v[30:33]
	v_mfma_f32_16x16x32_bf16 v[22:25], v[170:173], v[212:215], v[22:25]
	v_mfma_f32_16x16x32_bf16 v[14:17], v[178:181], v[212:215], v[14:17]
	s_setprio 0
	s_barrier
	s_add_u32 s20, s20, 0x80080
	s_addc_u32 s21, s21, 0
	s_add_i32 s22, s22, s27
	v_lshl_add_u64 v[166:167], s[20:21], 0, v[132:133]
	s_mov_b32 m0, s22
	s_nop 0
	global_load_lds_dwordx4 v[166:167], off
	v_lshl_add_u64 v[166:167], s[20:21], 0, v[130:131]
	s_add_i32 m0, s22, 0x2000
	s_nop 0
	global_load_lds_dwordx4 v[166:167], off
	s_cmp_eq_u32 s82, 0
	s_cbranch_scc1 .Lpb11_p8n
	s_waitcnt vmcnt(14)
	s_branch .Lpb11_p8j

; __device__ __forceinline__ unsigned cvt_pk_bf16(float lo, float hi) { unsigned r; asm volatile("v_cvt_pk_bf16_f32 %0, %1, %2" : "=v"(r) : "v"(lo), "v"(hi)); return r; }
; #define PG8_MMA(ai, bj, At, Bt) do { __builtin_amdgcn_s_setprio(1); _Pragma("unroll") for (int m = 0; m < 4; ++m) _Pragma("unroll") for (int n = 0; n < 2; ++n) _Pragma("unroll") for (int k = 0; k < 2; ++k) \
;         acc[ai][bj][m][n] = __builtin_amdgcn_mfma_f32_16x16x32_bf16(Bt[n][k], At[m][k], acc[ai][bj][m][n], 0, 0, 0); __builtin_amdgcn_s_setprio(0); } while (0)
; #define PG8_WAIT_V(n) asm volatile("s_waitcnt vmcnt(" #n ")" ::: "memory")
; #define PG8_BAR __builtin_amdgcn_s_barrier()
; template <class Epi, class Sched>
; __device__ __forceinline__ void gemm_phase(LAS unsigned char* lds, const int K, const Sched& S, const Epi& E) {
;     ...
;             PG8_WAIT_V(6); PG8_BAR; PG8_MMA(1, 1, At, B1); PG8_BAR;
;         }
;         E(acc, cur, wr, wc, fr, fq);
;         if (!has_next) break;
;     __device__ __forceinline__ void operator()(const f32x4 (&acc)[2][2][4][2], const Unit& u, int wr, int wc, int fr, int fq) const {
;         const int row0 = u.rbase + wr * 64 + fr, col0 = u.pn * BM + wc * 32 + 8 * fq;
; #pragma unroll
;         for (int ai = 0; ai < 2; ++ai)
; #pragma unroll
;             for (int m = 0; m < 4; ++m) { bf16_t* rowp = O + (size_t)(row0 + ai * HALF + m * 16) * ldc + col0;
; #pragma unroll
;                 for (int bj = 0; bj < 2; ++bj) { const f32x4 v0 = acc[ai][bj][m][0], v1 = acc[ai][bj][m][1];
;                     u32x4 w; w.x = cvt_pk_bf16(v0[0], v0[1]); w.y = cvt_pk_bf16(v0[2], v0[3]); w.z = cvt_pk_bf16(v1[0], v1[1]); w.w = cvt_pk_bf16(v1[2], v1[3]);
;                     *(u32x4*)(rowp + bj * HALF) = w; } }
.Lpb11_p8j:
	s_barrier
	s_setprio 1
	v_mfma_f32_16x16x32_bf16 v[50:53], v[216:219], v[182:185], v[50:53]
	v_mfma_f32_16x16x32_bf16 v[42:45], v[224:227], v[182:185], v[42:45]
	v_mfma_f32_16x16x32_bf16 v[34:37], v[216:219], v[190:193], v[34:37]
	v_mfma_f32_16x16x32_bf16 v[26:29], v[224:227], v[190:193], v[26:29]
	v_mfma_f32_16x16x32_bf16 v[18:21], v[216:219], v[198:201], v[18:21]
	v_mfma_f32_16x16x32_bf16 v[10:13], v[224:227], v[198:201], v[10:13]
	v_mfma_f32_16x16x32_bf16 v[6:9], v[216:219], v[208:211], v[6:9]
	v_mfma_f32_16x16x32_bf16 v[2:5], v[224:227], v[208:211], v[2:5]
	v_mfma_f32_16x16x32_bf16 v[50:53], v[220:223], v[186:189], v[50:53]
	v_mfma_f32_16x16x32_bf16 v[42:45], v[228:231], v[186:189], v[42:45]
	v_mfma_f32_16x16x32_bf16 v[34:37], v[220:223], v[194:197], v[34:37]
	v_mfma_f32_16x16x32_bf16 v[26:29], v[228:231], v[194:197], v[26:29]
	v_mfma_f32_16x16x32_bf16 v[18:21], v[220:223], v[202:205], v[18:21]
	v_mfma_f32_16x16x32_bf16 v[10:13], v[228:231], v[202:205], v[10:13]
	v_mfma_f32_16x16x32_bf16 v[6:9], v[220:223], v[212:215], v[6:9]
	v_mfma_f32_16x16x32_bf16 v[2:5], v[228:231], v[212:215], v[2:5]
	s_setprio 0
	s_add_i32 s46, s46, 2
	s_add_u32 s18, s18, 0x100
	s_addc_u32 s19, s19, 0
	s_cmp_gt_u32 s46, 29
	s_barrier
	s_cbranch_scc0 .LBB0_1290
	v_lshl_or_b32 v142, s44, 8, v157
	v_add_u32_e32 v134, s43, v155
	v_ashrrev_i32_e32 v143, 31, v142
	v_mov_b64_e32 v[140:141], s[10:11]
	v_mad_i64_i32 v[144:145], s[18:19], v134, s39, v[140:141]
	v_lshlrev_b64 v[142:143], 1, v[142:143]
	v_lshl_add_u64 v[144:145], v[144:145], 0, v[142:143]
	v_cvt_pk_bf16_f32 v126, v126, v127
	v_cvt_pk_bf16_f32 v127, v128, v129
	v_cvt_pk_bf16_f32 v128, v122, v123
	v_cvt_pk_bf16_f32 v129, v124, v125
	global_store_dwordx4 v[144:145], v[126:129], off
	v_cvt_pk_bf16_f32 v114, v114, v115
	v_cvt_pk_bf16_f32 v115, v116, v117
	v_cvt_pk_bf16_f32 v116, v106, v107
	v_add_u32_e32 v106, 16, v134
	v_mad_i64_i32 v[106:107], s[18:19], v106, s39, v[140:141]
	v_cvt_pk_bf16_f32 v117, v108, v109
	global_store_dwordx4 v[144:145], v[114:117], off offset:256
	s_and_b64 vcc, exec, s[0:1]
	s_mov_b32 s44, s16
	v_lshl_add_u64 v[114:115], v[106:107], 0, v[142:143]
	v_cvt_pk_bf16_f32 v106, v118, v119
	v_cvt_pk_bf16_f32 v107, v120, v121
	v_cvt_pk_bf16_f32 v108, v110, v111
	v_cvt_pk_bf16_f32 v109, v112, v113
	global_store_dwordx4 v[114:115], v[106:109], off
	v_cvt_pk_bf16_f32 v98, v98, v99
	v_cvt_pk_bf16_f32 v99, v100, v101
	v_cvt_pk_bf16_f32 v100, v90, v91
	v_add_u32_e32 v90, 32, v134
	v_mad_i64_i32 v[90:91], s[18:19], v90, s39, v[140:141]
	v_cvt_pk_bf16_f32 v101, v92, v93
	global_store_dwordx4 v[114:115], v[98:101], off offset:256
	s_mov_b32 s43, s41
	v_mov_b32_e32 v144, v164
	v_lshl_add_u64 v[98:99], v[90:91], 0, v[142:143]
	v_cvt_pk_bf16_f32 v90, v102, v103
	v_cvt_pk_bf16_f32 v91, v104, v105
	v_cvt_pk_bf16_f32 v92, v94, v95
	v_cvt_pk_bf16_f32 v93, v96, v97
	global_store_dwordx4 v[98:99], v[90:93], off
	v_cvt_pk_bf16_f32 v82, v82, v83
	v_cvt_pk_bf16_f32 v83, v84, v85
	v_cvt_pk_bf16_f32 v84, v74, v75
	v_add_u32_e32 v74, 48, v134
	v_mad_i64_i32 v[74:75], s[18:19], v74, s39, v[140:141]
	v_cvt_pk_bf16_f32 v85, v76, v77
	global_store_dwordx4 v[98:99], v[82:85], off offset:256
	s_nop 1
	v_lshl_add_u64 v[82:83], v[74:75], 0, v[142:143]
	v_cvt_pk_bf16_f32 v74, v86, v87
	v_cvt_pk_bf16_f32 v75, v88, v89
	v_cvt_pk_bf16_f32 v76, v78, v79
	v_cvt_pk_bf16_f32 v77, v80, v81
	global_store_dwordx4 v[82:83], v[74:77], off
	v_cvt_pk_bf16_f32 v70, v70, v71
	v_cvt_pk_bf16_f32 v71, v72, v73
	v_cvt_pk_bf16_f32 v72, v66, v67
	v_add_u32_e32 v66, 0x80, v134
	v_mad_i64_i32 v[66:67], s[18:19], v66, s39, v[140:141]
	v_lshl_add_u64 v[66:67], v[66:67], 0, v[142:143]
	v_cvt_pk_bf16_f32 v73, v68, v69
	global_store_dwordx4 v[82:83], v[70:73], off offset:256
	v_cvt_pk_bf16_f32 v62, v62, v63
	v_cvt_pk_bf16_f32 v63, v64, v65
	v_cvt_pk_bf16_f32 v64, v58, v59
	v_cvt_pk_bf16_f32 v65, v60, v61
	global_store_dwordx4 v[66:67], v[62:65], off
	v_cvt_pk_bf16_f32 v50, v50, v51
	v_cvt_pk_bf16_f32 v51, v52, v53
	v_cvt_pk_bf16_f32 v52, v42, v43
	v_add_u32_e32 v42, 0x90, v134
	v_mad_i64_i32 v[42:43], s[18:19], v42, s39, v[140:141]
	v_cvt_pk_bf16_f32 v53, v44, v45
	global_store_dwordx4 v[66:67], v[50:53], off offset:256
	s_nop 1
	v_lshl_add_u64 v[50:51], v[42:43], 0, v[142:143]
	v_cvt_pk_bf16_f32 v42, v54, v55
	v_cvt_pk_bf16_f32 v43, v56, v57
	v_cvt_pk_bf16_f32 v44, v46, v47
	v_cvt_pk_bf16_f32 v45, v48, v49
	global_store_dwordx4 v[50:51], v[42:45], off
	v_cvt_pk_bf16_f32 v34, v34, v35
	v_cvt_pk_bf16_f32 v35, v36, v37
	v_cvt_pk_bf16_f32 v36, v26, v27
	v_add_u32_e32 v26, 0xa0, v134
	v_mad_i64_i32 v[26:27], s[18:19], v26, s39, v[140:141]
	v_cvt_pk_bf16_f32 v37, v28, v29
	global_store_dwordx4 v[50:51], v[34:37], off offset:256
	s_nop 1
	v_lshl_add_u64 v[34:35], v[26:27], 0, v[142:143]
	v_cvt_pk_bf16_f32 v26, v38, v39
	v_cvt_pk_bf16_f32 v27, v40, v41
	v_cvt_pk_bf16_f32 v28, v30, v31
	v_cvt_pk_bf16_f32 v29, v32, v33
	global_store_dwordx4 v[34:35], v[26:29], off
	v_cvt_pk_bf16_f32 v18, v18, v19
	v_cvt_pk_bf16_f32 v19, v20, v21
	v_cvt_pk_bf16_f32 v20, v10, v11
	v_add_u32_e32 v10, 0xb0, v134
	v_mad_i64_i32 v[10:11], s[18:19], v10, s39, v[140:141]
	v_cvt_pk_bf16_f32 v21, v12, v13
	global_store_dwordx4 v[34:35], v[18:21], off offset:256
	v_mov_b32_e32 v141, v161
	v_mov_b32_e32 v140, v162
	v_lshl_add_u64 v[18:19], v[10:11], 0, v[142:143]
	v_mov_b32_e32 v142, v163
	s_mov_b64 s[18:19], s[2:3]
	v_cvt_pk_bf16_f32 v10, v22, v23
	v_cvt_pk_bf16_f32 v11, v24, v25
	v_cvt_pk_bf16_f32 v12, v14, v15
	v_cvt_pk_bf16_f32 v13, v16, v17
	global_store_dwordx4 v[18:19], v[10:13], off
	v_cvt_pk_bf16_f32 v6, v6, v7
	v_cvt_pk_bf16_f32 v7, v8, v9
	v_cvt_pk_bf16_f32 v8, v2, v3
	v_cvt_pk_bf16_f32 v9, v4, v5
	global_store_dwordx4 v[18:19], v[6:9], off offset:256
	s_cbranch_vccz .LBB0_1285
	s_waitcnt vmcnt(0)
	s_cmpk_gt_u32 s24, 0xff
	s_cbranch_scc1 .LBB0_1294
	s_barrier

; #define BG_I(x) bg_issue1<x>(bg, bgwg, bgNW, bglane)
; #define BG_F(y) bg_finish1<y, 32>(bg)
; __device__ __forceinline__ bool bg_decode(int st, int wg, int NW, int lane, KP kp, const float*& src, int& ldS, bf16_t*& dst, int& o2) {
;     ...
;     if (r < 65536) {
;         const int e = r >> 10, kc = (r >> 2) & 255, kind = (r >> 1) & 1, cc = r & 1, n = cc * 256 + lane;
;         ldS = FF; o2 = 256 * 8;
;         src = kp->in[27 + kind] + ((size_t)(l * NE + e) * D + kc * 8) * FF + n;
;         const int drow = (n >> 7) * 256 + kind * 128 + (n & 127);
;         dst = (bf16_t*)(ws + WS_WGU) + l * WGU_L + (size_t)e * 1024 * D + ((size_t)kc * 1024 + drow) * 8;
; __device__ __forceinline__ void hy_fft_phase(LAS unsigned char* lds, int bid, int G, const bf16_t* vgT, bf16_t* zT, const float* a3, const float* wout, const float* skip, float* filt, float4* gspec) {
;     ...
;     { const int nst = (BG_STEPS + bgNW - 1) / bgNW;
;       if (bg.st < nst) { BG_I(0);
; #pragma unroll 1
;         while (bg.st < nst) { BG_I(1); BG_F(0); BG_I(0); BG_F(1); }
;         bg_finish1<0, 0>(bg); } }
.Lpb11_d1:
	s_cmp_ge_u32 s70, 0x26000
	s_cbranch_scc1 .Lpb11_dend
	s_cmp_eq_u32 s80, 0
	s_cbranch_scc0 .Lpb11_adv3
	s_cmp_ge_u32 s70, 0x18000
	s_cselect_b32 s84, 0x18000, 0
	s_cselect_b32 s83, 0x10000000, 0
	s_mov_b32 s81, 0x4030000
	s_cselect_b32 s81, 0x14430000, s81
	s_sub_u32 s84, s70, s84
	s_lshr_b32 s85, s84, 2
	s_lshl_b32 s85, s85, 14
	s_and_b32 s86, s84, 1
	s_lshl_b32 s87, s86, 10
	s_add_u32 s87, s87, s85
	s_add_u32 s87, s87, s83
	s_bitcmp1_b32 s84, 1
	s_cselect_b64 s[72:73], s[76:77], s[74:75]
	s_add_u32 s72, s72, s87
	s_addc_u32 s73, s73, 0
	s_add_u32 s88, s72, 0x2000
	s_addc_u32 s89, s73, 0
	s_lshl_b32 s86, s86, 13
	s_add_u32 s85, s85, s86
	s_and_b32 s86, s84, 2
	s_lshl_b32 s86, s86, 10
	s_add_u32 s85, s85, s86
	s_add_u32 s85, s85, s81
	v_add_u32_e32 v253, s85, v252
	s_movk_i32 s81, 0x400
	s_branch .Lpb11_ld3

; __device__ __forceinline__ void xcd_barrier(const XcdBarrier& b) {
;     asm volatile("s_waitcnt vmcnt(0)" ::: "memory");
;     __syncthreads();
;     if (threadIdx.x == 0) {
;         unsigned* bar = b.bar;
;         __builtin_amdgcn_s_waitcnt(0);
;         unsigned nloc = b.st[0], nx = b.st[1];
;         if (nloc == 0u) { xcd_barrier_complete(bar, b.x, nloc, nx); b.st[0] = nloc; b.st[1] = nx; }
; template <int BANK> __device__ __forceinline__ void bg_issue1(BgState& b, int wg, int NW, int lane) {
;     ...
;     for (int i = 0; i < 8; ++i) { const float* p = src + (size_t)i * ldS;
;         asm volatile("global_load_dword %0, %4, off\n\tglobal_load_dword %1, %4, off offset:256\n\tglobal_load_dword %2, %4, off offset:512\n\tglobal_load_dword %3, %4, off offset:768"
;                      : "=&v"(b.r[(BANK * 8 + i) * 4 + 0]), "=&v"(b.r[(BANK * 8 + i) * 4 + 1]), "=&v"(b.r[(BANK * 8 + i) * 4 + 2]), "=&v"(b.r[(BANK * 8 + i) * 4 + 3]) : "v"(p) : "memory"); }
;     b.st += 1;
.Lpb11_ld3:
	global_load_dword v244, v238, s[72:73] nt
	global_load_dword v245, v239, s[72:73] nt
	global_load_dword v246, v240, s[72:73] nt
	global_load_dword v247, v241, s[72:73] nt
	global_load_dword v248, v238, s[88:89] nt
	global_load_dword v249, v239, s[88:89] nt
	global_load_dword v250, v240, s[88:89] nt
	global_load_dword v251, v241, s[88:89] nt
	s_add_u32 s80, s80, 1
	s_and_b32 s80, s80, 3
	s_cmp_eq_u32 s80, 0
	s_cselect_b32 s84, s71, 0
	s_add_u32 s70, s70, s84
	s_mov_b32 s82, 1
	s_branch .Lpb11_drain
.Lpb11_dend:
	s_waitcnt vmcnt(0)
	s_waitcnt vmcnt(0) lgkmcnt(0)
	s_barrier
	s_mov_b64 s[0:1], exec
	v_readlane_b32 s2, v254, 9
	v_readlane_b32 s3, v254, 10
	s_and_b64 s[2:3], s[0:1], s[2:3]
	s_xor_b64 s[0:1], s[2:3], s[0:1]
	s_mov_b64 exec, s[2:3]
	s_cbranch_execz .LBB0_1348
	s_add_i32 s2, 0, 0x21000
	v_mov_b32_e32 v1, s2
	s_waitcnt vmcnt(0) expcnt(0) lgkmcnt(0)
	ds_read_b32 v3, v1
	s_add_i32 s2, 0, 0x21004
	v_mov_b32_e32 v1, s2
	ds_read_b32 v1, v1
	s_waitcnt lgkmcnt(1)
	v_cmp_ne_u32_e32 vcc, 0, v3
	s_cbranch_vccnz .LBB0_1311
	v_readlane_b32 s2, v254, 2
	v_readlane_b32 s3, v254, 3
	s_load_dwordx2 s[6:7], s[2:3], 0x4
	v_readlane_b32 s10, v254, 6
	v_readlane_b32 s11, v254, 7
	s_add_u32 s2, s10, 0x1000
	s_addc_u32 s3, s11, 0
	s_add_u32 s4, s10, 0x1100
	s_addc_u32 s5, s11, 0
	v_readlane_b32 s12, v254, 4
	s_waitcnt lgkmcnt(0)
	s_mul_i32 s18, s6, s12
	s_add_u32 s6, s10, 0x1200
	s_mul_i32 s18, s18, s7
	s_addc_u32 s7, s11, 0
	s_add_u32 s10, s10, 0x1300
	s_addc_u32 s11, s11, 0
	s_mov_b32 s19, 1
	v_mov_b32_e32 v17, 0
	s_branch .LBB0_1299

; template <class Epi, class Sched>
; __device__ __forceinline__ void gemm_phase(LAS unsigned char* lds, const int K, const Sched& S, const Epi& E) {
;     const int tid = tid_fresh(), wid = __builtin_amdgcn_readfirstlane(tid >> 6), lane = tid & 63, wr = wid >> 2, wc = wid & 3, fr = lane & 15, fq = lane >> 4;
;     const int nt = K / BK;
;     int R0, C0, R1, C1; stage_rc(tid * 16, R0, C0); stage_rc(tid * 16 + 8192, R1, C1);
;     const int Rb0 = Epi::PERM ? ((R0 & ~31) + perm32(R0 & 31)) : R0, Rb1 = Epi::PERM ? ((R1 & ~31) + perm32(R1 & 31)) : R1;
;     const unsigned voffB0 = S.b_off(Rb0, C0), voffB1 = S.b_off(Rb1, C1);
;     const size_t kstep = (size_t)(BK * 2);
;     const size_t kstepB = S.b_kstep(), hstep = S.b_hstep();
;     const unsigned ldsw = (unsigned)wid * 1024u;
;     const int aoff = lds_byte(wr * 64 + fr, fq * 8), boff = lds_byte(wc * 32 + fr, fq * 8);
;     ...
;     Unit cur, nxt; int ui = 0;
;     if (!S.next(0, cur)) return;
;     f32x4 acc[2][2][4][2];
; #pragma unroll
;     for (int a = 0; a < 2; ++a)
; #pragma unroll
;         for (int b = 0; b < 2; ++b)
; #pragma unroll
;             for (int m = 0; m < 4; ++m)
; #pragma unroll
;                 for (int n = 0; n < 2; ++n) acc[a][b][m][n] = (f32x4){0.f, 0.f, 0.f, 0.f};
;     bf16x8 At[4][2], B0[2][2], B1[2][2];
;     const char* const gA = S.a_base();
;     unsigned c00, c01, c10, c11, n00, n01, n10, n11;
;     PG8_AOFFS(cur, c00, c01, c10, c11);
;     const char* cB = S.b_ptr(cur);
;     PG8_STAGE(PG8_SB(0, 0), cB, voffB0, voffB1); PG8_STAGE(PG8_SA(0, 0), gA, c00, c01); PG8_STAGE(PG8_SB(0, 1), cB + hstep, voffB0, voffB1); PG8_STAGE(PG8_SA(0, 1), gA, c10, c11);
;     if (wr == 1) PG8_BAR;
;     PG8_WAIT_V(4); PG8_BAR;
;     PG8_STAGE(PG8_SB(1, 0), cB + kstepB, voffB0, voffB1); PG8_STAGE(PG8_SA(1, 0), gA + kstep, c00, c01); PG8_STAGE(PG8_SB(1, 1), cB + hstep + kstepB, voffB0, voffB1);
;     PG8_WAIT_V(6); PG8_BAR;
;     __device__ __forceinline__ void a_off4(const Unit& u, int r0, int r1, unsigned& o00, unsigned& o01, unsigned& o10, unsigned& o11) const {
;         const int p0 = u.pm * BM + r0, p1 = u.pm * BM + r1, p2 = p0 + HALF, p3 = p1 + HALF;
;         if (u.e >= NE) { o00 = (unsigned)p0 * (unsigned)(D * 2); o01 = (unsigned)p1 * (unsigned)(D * 2); o10 = (unsigned)p2 * (unsigned)(D * 2); o11 = (unsigned)p3 * (unsigned)(D * 2); return; }
;         const int* lp = list + u.e * T;
.LBB0_1814:
	s_or_b64 exec, exec, s[0:1]
	v_readlane_b32 s0, v254, 0
	v_readlane_b32 s1, v254, 1
	s_lshl_b32 s29, s28, 2
	v_readlane_b32 s2, v254, 5
	v_mov_b32_e32 v6, v0
	s_waitcnt lgkmcnt(0)
	s_barrier
	v_readlane_b32 s84, v254, 0
	v_readlane_b32 s85, v254, 1
	s_nop 1
	s_load_dwordx2 s[74:75], s[84:85], 0xe8
	s_load_dwordx2 s[78:79], s[84:85], 0x118
	v_and_b32_e32 v252, 63, v0
	v_lshrrev_b32_e32 v253, 6, v0
	v_lshlrev_b32_e32 v238, 2, v252
	v_lshlrev_b32_e32 v252, 4, v252
	v_add_u32_e32 v239, 0x2000, v238
	v_add_u32_e32 v240, 0x4000, v238
	v_add_u32_e32 v241, 0x6000, v238
	v_readlane_b32 s86, v254, 4
	v_readlane_b32 s87, v255, 40
	v_readfirstlane_b32 s88, v253
	s_nop 3
	s_lshl_b32 s71, s86, 3
	s_lshl_b32 s87, s87, 3
	s_add_u32 s87, s87, s88
	s_add_u32 s70, s87, 0x2e000
	s_mov_b32 s80, 0
	s_mov_b32 s82, 0
	s_mov_b32 s90, 0
	s_waitcnt lgkmcnt(0)
	s_cmp_lt_i32 s2, s29
	s_nop 0
	v_readfirstlane_b32 s30, v6
	s_cbranch_scc0 .LBB0_1836
	v_ashrrev_i32_e32 v1, 31, v6
	v_lshrrev_b32_e32 v1, 26, v1
	v_add_u32_e32 v1, v6, v1
	v_ashrrev_i32_e32 v9, 6, v1
	v_bfe_i32 v1, v6, 27, 1
	v_lshlrev_b32_e32 v2, 4, v6
	v_lshrrev_b32_e32 v1, 22, v1
	v_add_u32_e32 v1, v2, v1
	v_and_b32_e32 v1, 0xfffffc00, v1
	v_sub_u32_e32 v1, v2, v1
	v_lshrrev_b32_e32 v3, 4, v1
	v_bitop3_b32 v10, v3, v1, 32 bitop3:0x6c
	v_ashrrev_i32_e32 v1, 31, v1
	v_lshrrev_b32_e32 v1, 26, v1
	s_load_dwordx2 s[0:1], s[0:1], 0x118
	v_lshlrev_b32_e32 v3, 3, v9
	v_add_u32_e32 v1, v10, v1
	v_and_b32_e32 v3, -16, v3
	v_ashrrev_i32_e32 v8, 6, v1
	v_add_u32_e32 v2, 0x2000, v2
	v_add_u32_e32 v1, v8, v3
	v_ashrrev_i32_e32 v3, 31, v2
	v_lshrrev_b32_e32 v3, 22, v3
	v_add_u32_e32 v3, v2, v3
	s_waitcnt lgkmcnt(0)
	s_add_u32 s31, s0, 0x3ec30000
	v_ashrrev_i32_e32 v11, 10, v3
	v_readlane_b32 s3, v254, 5
	s_addc_u32 s33, s1, 0
	v_mul_i32_i24_e32 v3, 0x400, v11
	s_and_b32 s2, s3, -4
	v_sub_u32_e32 v2, v2, v3
	s_add_i32 s2, s2, 0
	v_lshrrev_b32_e32 v3, 4, v2
	s_add_i32 s2, s2, 0x21160
	v_bitop3_b32 v12, v3, v2, 32 bitop3:0x6c
	v_mov_b32_e32 v3, s2
	ds_read_b32 v3, v3
	v_ashrrev_i32_e32 v4, 31, v12
	v_lshrrev_b32_e32 v4, 26, v4
	v_lshlrev_b32_e32 v2, 3, v11
	v_add_u32_e32 v4, v12, v4
	s_waitcnt lgkmcnt(0)
	v_lshlrev_b32_e32 v5, 2, v3
	v_add_u32_e32 v5, 0, v5
	v_add_u32_e32 v5, 0x21040, v5
	ds_read_b32 v5, v5
	v_and_b32_e32 v2, -16, v2
	v_ashrrev_i32_e32 v13, 6, v4
	s_ashr_i32 s8, s3, 2
	v_add_u32_e32 v146, v13, v2
	s_waitcnt lgkmcnt(0)
	v_sub_u32_e32 v2, s8, v5
	v_lshlrev_b32_e32 v7, 8, v2
	v_add_u32_e32 v2, v7, v1
	v_add_u32_e32 v4, v7, v146
	v_cmp_gt_i32_e32 vcc, 64, v3
	v_readfirstlane_b32 s6, v3
	v_add_u32_e32 v14, 0x80, v2
	v_add_u32_e32 v15, 0x80, v4
	s_cbranch_vccz .LBB0_1817
	s_lshl_b32 s2, s6, 13
	s_ashr_i32 s3, s2, 31
	s_lshl_b64 s[2:3], s[2:3], 2
	s_add_u32 s2, s31, s2
	s_addc_u32 s3, s33, s3
	v_ashrrev_i32_e32 v3, 31, v2
	v_lshl_add_u64 v[16:17], v[2:3], 2, s[2:3]
	v_ashrrev_i32_e32 v5, 31, v4
	v_lshl_add_u64 v[18:19], v[4:5], 2, s[2:3]
	global_load_dword v3, v[16:17], off
	global_load_dword v5, v[18:19], off
	global_load_dword v20, v[18:19], off offset:512
	global_load_dword v21, v[16:17], off offset:512
	s_lshl_b32 s2, s6, 2
	s_add_i32 s2, s2, 0
	s_add_i32 s2, s2, 0x21660
	v_mov_b32_e32 v16, s2
	s_waitcnt vmcnt(0)
	ds_read_b32 v17, v16
	v_lshlrev_b32_e32 v3, 12, v3
	v_lshlrev_b32_e32 v5, 12, v5
	v_lshlrev_b32_e32 v16, 12, v21
	v_lshlrev_b32_e32 v18, 12, v20
	s_waitcnt lgkmcnt(0)
	v_cmp_lt_i32_e32 vcc, v2, v17
	s_nop 1
	v_cndmask_b32_e32 v3, 0, v3, vcc
	v_cmp_lt_i32_e32 vcc, v4, v17
	s_nop 1
	v_cndmask_b32_e32 v5, 0, v5, vcc
	v_cmp_lt_i32_e32 vcc, v14, v17
	s_nop 1
	v_cndmask_b32_e32 v16, 0, v16, vcc
	v_cmp_lt_i32_e32 vcc, v15, v17
	s_nop 1
	v_cndmask_b32_e32 v17, 0, v18, vcc
	s_cbranch_execz .LBB0_1818
	s_branch .LBB0_1819

; #define PG8_STAGE(bufoff, gbase, v0, v1) do { \
;         __builtin_amdgcn_global_load_lds((const unsigned*)((const char*)(gbase) + (v0)), (LAS unsigned*)(lds + (bufoff) + ldsw), 16, 0, 0); \
;         __builtin_amdgcn_global_load_lds((const unsigned*)((const char*)(gbase) + (v1)), (LAS unsigned*)(lds + (bufoff) + ldsw + 8192), 16, 0, 0); } while (0)
; #define PG8_LDA(dst, b, h) do { _Pragma("unroll") for (int m = 0; m < 4; ++m) _Pragma("unroll") for (int k = 0; k < 2; ++k) dst[m][k] = *(const LAS bf16x8*)(lds + PG8_SA(b, h) + aoff + m * 2048 + k * 1024); } while (0)
; #define PG8_LDB(dst, b, h) do { _Pragma("unroll") for (int n = 0; n < 2; ++n) _Pragma("unroll") for (int k = 0; k < 2; ++k) dst[n][k] = *(const LAS bf16x8*)(lds + PG8_SB(b, h) + boff + n * 2048 + k * 1024); } while (0)
; #define PG8_MMA(ai, bj, At, Bt) do { __builtin_amdgcn_s_setprio(1); _Pragma("unroll") for (int m = 0; m < 4; ++m) _Pragma("unroll") for (int n = 0; n < 2; ++n) _Pragma("unroll") for (int k = 0; k < 2; ++k) \
;         acc[ai][bj][m][n] = __builtin_amdgcn_mfma_f32_16x16x32_bf16(Bt[n][k], At[m][k], acc[ai][bj][m][n], 0, 0, 0); __builtin_amdgcn_s_setprio(0); } while (0)
; #define PG8_WAIT_V(n) asm volatile("s_waitcnt vmcnt(" #n ")" ::: "memory")
; #define PG8_BAR __builtin_amdgcn_s_barrier()
; #define PG8_SCHED __builtin_amdgcn_sched_barrier(0)
; template <class Epi, class Sched>
; __device__ __forceinline__ void gemm_phase(LAS unsigned char* lds, const int K, const Sched& S, const Epi& E) {
;     ...
;             PG8_WAIT_V(6); PG8_BAR; PG8_MMA(1, 1, At, B1); PG8_BAR;
;             PG8_LDB(B0, 1, 0); PG8_SCHED; PG8_LDA(At, 1, 0); PG8_STAGE(PG8_SA(0, 1), a2, x10, x11);
; __device__ __forceinline__ bool bg_decode(int st, int wg, int NW, int lane, KP kp, const float*& src, int& ldS, bf16_t*& dst, int& o2) {
;     ...
;         const int r2 = r - 65536, e = r2 >> 9, kc = (r2 >> 3) & 63, cc = r2 & 7, n = cc * 256 + lane;
;         ldS = D; o2 = 128 * 8;
;         src = kp->in[29] + ((size_t)(l * NE + e) * FF + kc * 8) * D + n;
;         dst = (bf16_t*)(ws + WS_WD) + l * WD_L + (size_t)e * D * FF + ((size_t)kc * D + n) * 8;
.Lpb17_p4j:
	s_barrier
	s_setprio 1
	v_mfma_f32_16x16x32_bf16 v[54:57], v[208:211], v[176:179], v[54:57]
	v_mfma_f32_16x16x32_bf16 v[50:53], v[216:219], v[176:179], v[50:53]
	v_mfma_f32_16x16x32_bf16 v[38:41], v[208:211], v[184:187], v[38:41]
	v_mfma_f32_16x16x32_bf16 v[34:37], v[216:219], v[184:187], v[34:37]
	v_mfma_f32_16x16x32_bf16 v[22:25], v[208:211], v[192:195], v[22:25]
	v_mfma_f32_16x16x32_bf16 v[18:21], v[216:219], v[192:195], v[18:21]
	v_mfma_f32_16x16x32_bf16 v[6:9], v[208:211], v[200:203], v[6:9]
	v_mfma_f32_16x16x32_bf16 v[2:5], v[216:219], v[200:203], v[2:5]
	v_mfma_f32_16x16x32_bf16 v[54:57], v[212:215], v[180:183], v[54:57]
	v_mfma_f32_16x16x32_bf16 v[50:53], v[220:223], v[180:183], v[50:53]
	v_mfma_f32_16x16x32_bf16 v[38:41], v[212:215], v[188:191], v[38:41]
	v_mfma_f32_16x16x32_bf16 v[34:37], v[220:223], v[188:191], v[34:37]
	v_mfma_f32_16x16x32_bf16 v[22:25], v[212:215], v[196:199], v[22:25]
	v_mfma_f32_16x16x32_bf16 v[18:21], v[220:223], v[196:199], v[18:21]
	v_mfma_f32_16x16x32_bf16 v[6:9], v[212:215], v[204:207], v[6:9]
	v_mfma_f32_16x16x32_bf16 v[2:5], v[220:223], v[204:207], v[2:5]
	s_setprio 0
	s_add_i32 s54, 0, 0x18000
	v_add_u32_e32 v134, s54, v149
	s_barrier
	ds_read_b128 v[160:163], v134
	ds_read_b128 v[164:167], v134 offset:1024
	ds_read_b128 v[168:171], v134 offset:2048
	ds_read_b128 v[172:175], v134 offset:3072
	s_mov_b32 m0, s39
	ds_read_b128 v[176:179], v151 offset:32768
	ds_read_b128 v[180:183], v151 offset:33792
	ds_read_b128 v[184:187], v151 offset:34816
	ds_read_b128 v[188:191], v151 offset:35840
	ds_read_b128 v[192:195], v151 offset:36864
	ds_read_b128 v[196:199], v151 offset:37888
	ds_read_b128 v[200:203], v151 offset:38912
	ds_read_b128 v[204:207], v151 offset:39936
	v_cndmask_b32_e32 v134, v140, v153, vcc
	global_load_lds_dwordx4 v139, s[26:27]
	s_mov_b32 m0, s40
	s_nop 0
	global_load_lds_dwordx4 v134, s[26:27]
	s_add_u32 s90, s90, 1
	s_cmp_lt_u32 s90, 4
	s_cbranch_scc1 .Lpb17_p5n
	s_mov_b32 s90, 0
	s_cmp_ge_u32 s70, 0x30000
	s_cbranch_scc1 .Lpb17_p5n
	s_cmp_eq_u32 s80, 0
	s_cbranch_scc0 .Lpb17_adv8
	s_cmp_ge_u32 s70, 0x28000
	s_mov_b32 s84, 0x10000
	s_cselect_b32 s84, 0x28000, s84
	s_cselect_b32 s83, 0x10000000, 0
	s_mov_b32 s81, 0x24830000
	s_cselect_b32 s81, 0x2ca30000, s81
	s_sub_u32 s84, s70, s84
	s_lshr_b32 s85, s84, 3
	s_and_b32 s86, s84, 7
	s_lshl_b32 s87, s85, 16
	s_lshl_b32 s84, s86, 10
	s_add_u32 s87, s87, s84
	s_add_u32 s87, s87, s83
	s_add_u32 s72, s74, s87
	s_addc_u32 s73, s75, 0
	s_add_u32 s88, s72, 0x8000
	s_addc_u32 s89, s73, 0
	s_lshl_b32 s85, s85, 15
	s_lshl_b32 s86, s86, 12
	s_add_u32 s85, s85, s86
	s_add_u32 s85, s85, s81
	v_add_u32_e32 v253, s85, v252
	s_branch .Lpb17_ld8
